# RG-LRU: odd waves run the next chunk's MFMAs right after the exchange barrier (skew between the two waves of a SIMD if waves are placed pairwise)
# speedup vs baseline: 1.0087x; 1.0087x over previous
.LBB0_1451:
	s_load_dwordx4 s[0:3], s[8:9], 0x138
	s_waitcnt lgkmcnt(0)
	s_mov_b64 s[4:5], s[0:1]
	s_cmp_lt_i32 s4, 12
	s_cselect_b64 s[0:1], -1, 0
	s_cmp_gt_i32 s5, 11
	s_cselect_b64 s[2:3], -1, 0
	s_and_b64 s[0:1], s[0:1], s[2:3]
	s_andn2_b64 vcc, exec, s[0:1]
	s_cbranch_vccnz .LBB0_1535
	s_mov_b64 s[24:25], s[8:9]
	v_mbcnt_lo_u32_b32 v202, -1, 0
	v_mbcnt_hi_u32_b32 v202, -1, v202
	s_load_dword s0, s[8:9], 0x148
	s_waitcnt lgkmcnt(0)
	v_writelane_b32 v241, s0, 18
	s_nop 1
	v_writelane_b32 v241, s1, 19
	s_add_u32 s0, s8, 0x148
	s_addc_u32 s1, s9, 0
	v_writelane_b32 v241, s0, 34
	s_nop 1
	v_writelane_b32 v241, s1, 35
	v_readlane_b32 s0, v243, 0
	s_cmpk_gt_i32 s0, 0xff
	v_readlane_b32 s1, v243, 1
	s_cbranch_scc1 .LBB0_1482
	v_readlane_b32 s0, v243, 7
	v_readlane_b32 s1, v243, 8
	v_readlane_b32 s4, v243, 0
	v_readlane_b32 s6, v243, 12
	s_load_dwordx2 s[2:3], s[0:1], 0x130
	s_lshr_b32 s7, s6, 2
	s_and_b32 s14, s6, 1
	s_and_b32 s8, s6, 3
	s_bfe_u32 s11, s4, 0x20003
	s_lshr_b32 s50, s4, 5
	s_lshl_b32 s50, s50, 3
	s_and_b32 s51, s4, 7
	s_or_b32 s50, s50, s51
	s_lshr_b32 s9, s50, 2
	s_and_b32 s10, s50, 3
	v_and_b32_e32 v160, 15, v202
	v_lshrrev_b32_e32 v161, 4, v202
	v_lshlrev_b32_e32 v209, 2, v202
	s_lshl_b32 s50, s7, 15
	v_xor_b32_e32 v178, v161, v160
	v_lshlrev_b32_e32 v178, 4, v178
	v_lshl_add_u32 v162, v160, 9, v178
	v_add_u32_e32 v162, s50, v162
	s_lshl_b32 s51, s11, 6
	s_lshl_b32 s52, s8, 4
	s_add_i32 s51, s51, s52
	v_add_u32_e32 v179, s51, v160
	v_lshrrev_b32_e32 v180, 3, v179
	v_and_b32_e32 v181, 7, v179
	v_lshlrev_b32_e32 v181, 1, v181
	v_lshlrev_b32_e32 v182, 2, v161
	v_add_u32_e32 v183, 0, v182
	v_xor_b32_e32 v184, v180, v183
	v_lshlrev_b32_e32 v184, 4, v184
	v_lshl_add_u32 v184, v183, 9, v184
	v_add3_u32 v165, v184, v181, s50
	v_add_u32_e32 v183, 1, v182
	v_xor_b32_e32 v184, v180, v183
	v_lshlrev_b32_e32 v184, 4, v184
	v_lshl_add_u32 v184, v183, 9, v184
	v_add3_u32 v166, v184, v181, s50
	v_add_u32_e32 v183, 2, v182
	v_xor_b32_e32 v184, v180, v183
	v_lshlrev_b32_e32 v184, 4, v184
	v_lshl_add_u32 v184, v183, 9, v184
	v_add3_u32 v167, v184, v181, s50
	v_add_u32_e32 v183, 3, v182
	v_xor_b32_e32 v184, v180, v183
	v_lshlrev_b32_e32 v184, 4, v184
	v_lshl_add_u32 v184, v183, 9, v184
	v_add3_u32 v168, v184, v181, s50
	v_lshrrev_b32_e32 v185, 5, v202
	v_and_b32_e32 v186, 31, v202
	s_lshl_b32 s51, s6, 4
	v_add_u32_e32 v187, 0, v185
	v_xor_b32_e32 v188, v186, v187
	v_lshlrev_b32_e32 v188, 4, v188
	v_add_u32_e32 v187, s51, v187
	v_lshl_add_u32 v211, v187, 11, v188
	v_add_u32_e32 v187, 2, v185
	v_xor_b32_e32 v188, v186, v187
	v_lshlrev_b32_e32 v188, 4, v188
	v_add_u32_e32 v187, s51, v187
	v_lshl_add_u32 v212, v187, 11, v188
	v_add_u32_e32 v187, 4, v185
	v_xor_b32_e32 v188, v186, v187
	v_lshlrev_b32_e32 v188, 4, v188
	v_add_u32_e32 v187, s51, v187
	v_lshl_add_u32 v213, v187, 11, v188
	v_add_u32_e32 v187, 6, v185
	v_xor_b32_e32 v188, v186, v187
	v_lshlrev_b32_e32 v188, 4, v188
	v_add_u32_e32 v187, s51, v187
	v_lshl_add_u32 v214, v187, 11, v188
	v_add_u32_e32 v187, 8, v185
	v_xor_b32_e32 v188, v186, v187
	v_lshlrev_b32_e32 v188, 4, v188
	v_add_u32_e32 v187, s51, v187
	v_lshl_add_u32 v215, v187, 11, v188
	v_add_u32_e32 v187, 10, v185
	v_xor_b32_e32 v188, v186, v187
	v_lshlrev_b32_e32 v188, 4, v188
	v_add_u32_e32 v187, s51, v187
	v_lshl_add_u32 v216, v187, 11, v188
	v_add_u32_e32 v187, 12, v185
	v_xor_b32_e32 v188, v186, v187
	v_lshlrev_b32_e32 v188, 4, v188
	v_add_u32_e32 v187, s51, v187
	v_lshl_add_u32 v217, v187, 11, v188
	v_add_u32_e32 v187, 14, v185
	v_xor_b32_e32 v188, v186, v187
	v_lshlrev_b32_e32 v188, 4, v188
	v_add_u32_e32 v187, s51, v187
	v_lshl_add_u32 v218, v187, 11, v188
	s_lshl_b32 s51, s6, 7
	s_add_i32 s51, s51, 0x20000
	v_lshl_add_u32 v207, v160, 3, s51
	s_lshl_b32 s51, s8, 7
	s_add_i32 s51, s51, 0x20000
	v_lshl_add_u32 v208, v160, 3, s51
	s_lshl_b32 s51, s7, 6
	v_add_u32_e32 v189, s51, v182
	s_lshl_b32 s51, s8, 4
	v_add_u32_e32 v190, s51, v160
	v_lshlrev_b32_e32 v190, 1, v190
	v_lshl_add_u32 v210, v189, 11, v190
	s_waitcnt lgkmcnt(0)
	s_lshl_b32 s50, s10, 9
	s_add_u32 s16, s2, s50
	s_addc_u32 s17, s3, 0
	s_add_u32 s16, s16, 0x1b900000
	s_addc_u32 s17, s17, 0
	s_lshl_b32 s50, s10, 9
	s_lshl_b32 s51, s11, 7
	s_add_i32 s50, s50, s51
	s_add_u32 s18, s2, s50
	s_addc_u32 s19, s3, 0
	s_add_u32 s18, s18, 0x13100000
	s_addc_u32 s19, s19, 0
	s_add_u32 s20, s2, s50
	s_addc_u32 s21, s3, 0
	s_add_u32 s20, s20, 0x29100000
	s_addc_u32 s21, s21, 0
	s_lshl_b32 s50, s4, 18
	s_add_u32 s22, s2, s50
	s_addc_u32 s23, s3, 0
	s_add_u32 s22, s22, 0x20100000
	s_addc_u32 s23, s23, 0
	s_lshl_b32 s50, s10, 10
	s_lshl_b32 s51, s11, 6
	s_add_i32 s50, s50, s51
	s_lshl_b32 s51, s8, 4
	s_add_i32 s50, s50, s51
	s_add_i32 s50, s50, 0
	s_lshl_b32 s50, s50, 9
	s_add_u32 s46, s2, s50
	s_addc_u32 s47, s3, 0
	s_add_u32 s46, s46, 0x1000000
	s_addc_u32 s47, s47, 0
	s_add_u32 s48, s46, 0x20000
	s_addc_u32 s49, s47, 0
	v_lshlrev_b32_e32 v178, 9, v160
	v_lshl_add_u32 v178, v161, 4, v178
	global_load_dwordx4 v[0:3], v178, s[46:47]
	global_load_dwordx4 v[4:7], v178, s[46:47] offset:64
	global_load_dwordx4 v[8:11], v178, s[46:47] offset:128
	global_load_dwordx4 v[12:15], v178, s[46:47] offset:192
	global_load_dwordx4 v[16:19], v178, s[46:47] offset:256
	global_load_dwordx4 v[20:23], v178, s[46:47] offset:320
	global_load_dwordx4 v[24:27], v178, s[46:47] offset:384
	global_load_dwordx4 v[28:31], v178, s[46:47] offset:448
	global_load_dwordx4 v[32:35], v178, s[48:49]
	global_load_dwordx4 v[36:39], v178, s[48:49] offset:64
	global_load_dwordx4 v[40:43], v178, s[48:49] offset:128
	global_load_dwordx4 v[44:47], v178, s[48:49] offset:192
	global_load_dwordx4 v[48:51], v178, s[48:49] offset:256
	global_load_dwordx4 v[52:55], v178, s[48:49] offset:320
	global_load_dwordx4 v[56:59], v178, s[48:49] offset:384
	global_load_dwordx4 v[60:63], v178, s[48:49] offset:448
	s_load_dwordx2 s[46:47], s[0:1], 0xa0
	s_load_dwordx2 s[48:49], s[0:1], 0xb0
	s_load_dwordx2 s[40:41], s[0:1], 0xb8
	s_lshl_b32 s50, s10, 8
	s_lshl_b32 s51, s11, 6
	s_add_i32 s50, s50, s51
	s_lshl_b32 s51, s8, 4
	s_add_i32 s50, s50, s51
	v_add_u32_e32 v179, s50, v160
	v_lshlrev_b32_e32 v179, 2, v179
	s_waitcnt lgkmcnt(0)
	global_load_dword v173, v179, s[46:47]
	global_load_dword v174, v179, s[48:49]
	global_load_dword v175, v179, s[40:41]
	v_cmp_le_u32_e64 s[34:35], 16, v202
	v_cmp_le_u32_e64 s[36:37], 32, v202
	v_add_u32_e32 v204, -16, v202
	v_add_u32_e32 v205, -32, v202
	v_add_u32_e32 v206, 48, v160
	s_cmp_eq_u32 s7, 1
	s_cselect_b64 s[38:39], -1, 0
	v_and_b32_e32 v204, 63, v204
	v_lshlrev_b32_e32 v204, 2, v204
	v_and_b32_e32 v205, 63, v205
	v_lshlrev_b32_e32 v205, 2, v205
	v_and_b32_e32 v206, 63, v206
	v_lshlrev_b32_e32 v206, 2, v206
	v_mov_b32_e32 v176, 0
	s_mov_b32 s53, 0xbfb8aa3b
	s_waitcnt vmcnt(0)
	v_mul_f32_e32 v173, s53, v173
	v_mul_f32_e32 v174, s53, v174
	v_mul_f32_e32 v175, s53, v175
	v_exp_f32_e32 v175, v175
	s_nop 0
	v_add_f32_e32 v180, 1.0, v175
	v_log_f32_e32 v180, v180
	v_mov_b32_e32 v181, 0x3eaaaaab
	v_fma_f32 v181, v175, v181, -0.5
	v_fma_f32 v181, v175, v181, 1.0
	v_mul_f32_e32 v181, v175, v181
	v_mul_f32_e32 v181, 0x3fb8aa3b, v181
	v_cmp_gt_f32_e32 vcc, 0x3cf5c28f, v175
	s_nop 1
	v_cndmask_b32_e32 v175, v180, v181, vcc
	v_mul_f32_e32 v175, 0xc1000000, v175
	s_mov_b32 s13, 0
	s_barrier
	s_cmp_lt_u32 s13, 2
	s_lshl_b32 s50, s13, 7
	s_lshl_b32 s51, s9, 8
	s_add_i32 s51, s51, 0x8000
	s_add_i32 s51, s51, s50
	s_lshl_b32 s59, s9, 11
	s_add_i32 s59, s59, s50
	s_addk_i32 s59, 0xff00
	s_cmp_lt_u32 s13, 2
	s_cselect_b32 s59, s51, s59
	s_lshl_b32 s52, s59, 11
	s_add_u32 s46, s16, s52
	s_addc_u32 s47, s17, 0
	s_lshl_b32 s52, s6, 13
	s_mov_b32 m0, s52
	s_add_i32 s52, s52, 0x400
	global_load_lds_dwordx4 v211, s[46:47]
	s_mov_b32 m0, s52
	s_add_i32 s52, s52, 0x400
	global_load_lds_dwordx4 v212, s[46:47]
	s_mov_b32 m0, s52
	s_add_i32 s52, s52, 0x400
	global_load_lds_dwordx4 v213, s[46:47]
	s_mov_b32 m0, s52
	s_add_i32 s52, s52, 0x400
	global_load_lds_dwordx4 v214, s[46:47]
	s_mov_b32 m0, s52
	s_add_i32 s52, s52, 0x400
	global_load_lds_dwordx4 v215, s[46:47]
	s_mov_b32 m0, s52
	s_add_i32 s52, s52, 0x400
	global_load_lds_dwordx4 v216, s[46:47]
	s_mov_b32 m0, s52
	s_add_i32 s52, s52, 0x400
	global_load_lds_dwordx4 v217, s[46:47]
	s_mov_b32 m0, s52
	s_nop 0
	global_load_lds_dwordx4 v218, s[46:47]
	s_mov_b32 s58, 1
	s_cmp_lt_u32 s58, 2
	s_lshl_b32 s50, s58, 7
	s_lshl_b32 s51, s9, 8
	s_add_i32 s51, s51, 0x8000
	s_add_i32 s51, s51, s50
	s_lshl_b32 s59, s9, 11
	s_add_i32 s59, s59, s50
	s_addk_i32 s59, 0xff00
	s_cmp_lt_u32 s58, 2
	s_cselect_b32 s59, s51, s59
	s_lshl_b32 s52, s59, 11
	s_add_u32 s46, s16, s52
	s_addc_u32 s47, s17, 0
	s_lshl_b32 s52, s6, 13
	s_add_i32 s52, s52, 0x10000
	s_mov_b32 m0, s52
	s_add_i32 s52, s52, 0x400
	global_load_lds_dwordx4 v211, s[46:47]
	s_mov_b32 m0, s52
	s_add_i32 s52, s52, 0x400
	global_load_lds_dwordx4 v212, s[46:47]
	s_mov_b32 m0, s52
	s_add_i32 s52, s52, 0x400
	global_load_lds_dwordx4 v213, s[46:47]
	s_mov_b32 m0, s52
	s_add_i32 s52, s52, 0x400
	global_load_lds_dwordx4 v214, s[46:47]
	s_mov_b32 m0, s52
	s_add_i32 s52, s52, 0x400
	global_load_lds_dwordx4 v215, s[46:47]
	s_mov_b32 m0, s52
	s_add_i32 s52, s52, 0x400
	global_load_lds_dwordx4 v216, s[46:47]
	s_mov_b32 m0, s52
	s_add_i32 s52, s52, 0x400
	global_load_lds_dwordx4 v217, s[46:47]
	s_mov_b32 m0, s52
	s_nop 0
	global_load_lds_dwordx4 v218, s[46:47]
	s_waitcnt vmcnt(8)
	s_barrier
	s_cmp_eq_u32 s14, 0
	s_cbranch_scc1 .Lmylru_p0_0
	v_mov_b32_e32 v163, v162
	ds_read_b128 v[112:115], v163
	ds_read_b128 v[116:119], v163 offset:8192
	ds_read_b128 v[120:123], v163 offset:16384
	ds_read_b128 v[124:127], v163 offset:24576
	s_waitcnt lgkmcnt(3)
	v_mfma_f32_16x16x32_bf16 v[64:67], v[112:115], v[0:3], 0
	v_mfma_f32_16x16x32_bf16 v[68:71], v[112:115], v[32:35], 0
	v_xor_b32_e32 v164, 0x40, v163
	ds_read_b128 v[112:115], v164
	s_waitcnt lgkmcnt(3)
	v_mfma_f32_16x16x32_bf16 v[72:75], v[116:119], v[0:3], 0
	v_mfma_f32_16x16x32_bf16 v[76:79], v[116:119], v[32:35], 0
	ds_read_b128 v[116:119], v164 offset:8192
	s_waitcnt lgkmcnt(3)
	v_mfma_f32_16x16x32_bf16 v[80:83], v[120:123], v[0:3], 0
	v_mfma_f32_16x16x32_bf16 v[84:87], v[120:123], v[32:35], 0
	ds_read_b128 v[120:123], v164 offset:16384
	s_waitcnt lgkmcnt(3)
	v_mfma_f32_16x16x32_bf16 v[88:91], v[124:127], v[0:3], 0
	v_mfma_f32_16x16x32_bf16 v[92:95], v[124:127], v[32:35], 0
	ds_read_b128 v[124:127], v164 offset:24576
	s_waitcnt lgkmcnt(3)
	v_mfma_f32_16x16x32_bf16 v[64:67], v[112:115], v[4:7], v[64:67]
	v_mfma_f32_16x16x32_bf16 v[68:71], v[112:115], v[36:39], v[68:71]
	v_xor_b32_e32 v164, 0x80, v163
	ds_read_b128 v[112:115], v164
	s_waitcnt lgkmcnt(3)
	v_mfma_f32_16x16x32_bf16 v[72:75], v[116:119], v[4:7], v[72:75]
	v_mfma_f32_16x16x32_bf16 v[76:79], v[116:119], v[36:39], v[76:79]
	ds_read_b128 v[116:119], v164 offset:8192
	s_waitcnt lgkmcnt(3)
	v_mfma_f32_16x16x32_bf16 v[80:83], v[120:123], v[4:7], v[80:83]
	v_mfma_f32_16x16x32_bf16 v[84:87], v[120:123], v[36:39], v[84:87]
	ds_read_b128 v[120:123], v164 offset:16384
	s_waitcnt lgkmcnt(3)
	v_mfma_f32_16x16x32_bf16 v[88:91], v[124:127], v[4:7], v[88:91]
	v_mfma_f32_16x16x32_bf16 v[92:95], v[124:127], v[36:39], v[92:95]
	ds_read_b128 v[124:127], v164 offset:24576
	s_waitcnt lgkmcnt(3)
	v_mfma_f32_16x16x32_bf16 v[64:67], v[112:115], v[8:11], v[64:67]
	v_mfma_f32_16x16x32_bf16 v[68:71], v[112:115], v[40:43], v[68:71]
	v_xor_b32_e32 v164, 0xc0, v163
	ds_read_b128 v[112:115], v164
	s_waitcnt lgkmcnt(3)
	v_mfma_f32_16x16x32_bf16 v[72:75], v[116:119], v[8:11], v[72:75]
	v_mfma_f32_16x16x32_bf16 v[76:79], v[116:119], v[40:43], v[76:79]
	ds_read_b128 v[116:119], v164 offset:8192
	s_waitcnt lgkmcnt(3)
	v_mfma_f32_16x16x32_bf16 v[80:83], v[120:123], v[8:11], v[80:83]
	v_mfma_f32_16x16x32_bf16 v[84:87], v[120:123], v[40:43], v[84:87]
	ds_read_b128 v[120:123], v164 offset:16384
	s_waitcnt lgkmcnt(3)
	v_mfma_f32_16x16x32_bf16 v[88:91], v[124:127], v[8:11], v[88:91]
	v_mfma_f32_16x16x32_bf16 v[92:95], v[124:127], v[40:43], v[92:95]
	ds_read_b128 v[124:127], v164 offset:24576
	s_waitcnt lgkmcnt(3)
	v_mfma_f32_16x16x32_bf16 v[64:67], v[112:115], v[12:15], v[64:67]
	v_mfma_f32_16x16x32_bf16 v[68:71], v[112:115], v[44:47], v[68:71]
	v_xor_b32_e32 v164, 0x100, v163
	ds_read_b128 v[112:115], v164
	s_waitcnt lgkmcnt(3)
	v_mfma_f32_16x16x32_bf16 v[72:75], v[116:119], v[12:15], v[72:75]
	v_mfma_f32_16x16x32_bf16 v[76:79], v[116:119], v[44:47], v[76:79]
	ds_read_b128 v[116:119], v164 offset:8192
	s_waitcnt lgkmcnt(3)
	v_mfma_f32_16x16x32_bf16 v[80:83], v[120:123], v[12:15], v[80:83]
	v_mfma_f32_16x16x32_bf16 v[84:87], v[120:123], v[44:47], v[84:87]
	ds_read_b128 v[120:123], v164 offset:16384
	s_waitcnt lgkmcnt(3)
	v_mfma_f32_16x16x32_bf16 v[88:91], v[124:127], v[12:15], v[88:91]
	v_mfma_f32_16x16x32_bf16 v[92:95], v[124:127], v[44:47], v[92:95]
	ds_read_b128 v[124:127], v164 offset:24576
	s_waitcnt lgkmcnt(3)
	v_mfma_f32_16x16x32_bf16 v[64:67], v[112:115], v[16:19], v[64:67]
	v_mfma_f32_16x16x32_bf16 v[68:71], v[112:115], v[48:51], v[68:71]
	v_xor_b32_e32 v164, 0x140, v163
	ds_read_b128 v[112:115], v164
	s_waitcnt lgkmcnt(3)
	v_mfma_f32_16x16x32_bf16 v[72:75], v[116:119], v[16:19], v[72:75]
	v_mfma_f32_16x16x32_bf16 v[76:79], v[116:119], v[48:51], v[76:79]
	ds_read_b128 v[116:119], v164 offset:8192
	s_waitcnt lgkmcnt(3)
	v_mfma_f32_16x16x32_bf16 v[80:83], v[120:123], v[16:19], v[80:83]
	v_mfma_f32_16x16x32_bf16 v[84:87], v[120:123], v[48:51], v[84:87]
	ds_read_b128 v[120:123], v164 offset:16384
	s_waitcnt lgkmcnt(3)
	v_mfma_f32_16x16x32_bf16 v[88:91], v[124:127], v[16:19], v[88:91]
	v_mfma_f32_16x16x32_bf16 v[92:95], v[124:127], v[48:51], v[92:95]
	ds_read_b128 v[124:127], v164 offset:24576
	s_waitcnt lgkmcnt(3)
	v_mfma_f32_16x16x32_bf16 v[64:67], v[112:115], v[20:23], v[64:67]
	v_mfma_f32_16x16x32_bf16 v[68:71], v[112:115], v[52:55], v[68:71]
	v_xor_b32_e32 v164, 0x180, v163
	ds_read_b128 v[112:115], v164
	s_waitcnt lgkmcnt(3)
	v_mfma_f32_16x16x32_bf16 v[72:75], v[116:119], v[20:23], v[72:75]
	v_mfma_f32_16x16x32_bf16 v[76:79], v[116:119], v[52:55], v[76:79]
	ds_read_b128 v[116:119], v164 offset:8192
	s_waitcnt lgkmcnt(3)
	v_mfma_f32_16x16x32_bf16 v[80:83], v[120:123], v[20:23], v[80:83]
	v_mfma_f32_16x16x32_bf16 v[84:87], v[120:123], v[52:55], v[84:87]
	ds_read_b128 v[120:123], v164 offset:16384
	s_waitcnt lgkmcnt(3)
	v_mfma_f32_16x16x32_bf16 v[88:91], v[124:127], v[20:23], v[88:91]
	v_mfma_f32_16x16x32_bf16 v[92:95], v[124:127], v[52:55], v[92:95]
	ds_read_b128 v[124:127], v164 offset:24576
	s_waitcnt lgkmcnt(3)
	v_mfma_f32_16x16x32_bf16 v[64:67], v[112:115], v[24:27], v[64:67]
	v_mfma_f32_16x16x32_bf16 v[68:71], v[112:115], v[56:59], v[68:71]
	v_xor_b32_e32 v164, 0x1c0, v163
	ds_read_b128 v[112:115], v164
	s_waitcnt lgkmcnt(3)
	v_mfma_f32_16x16x32_bf16 v[72:75], v[116:119], v[24:27], v[72:75]
	v_mfma_f32_16x16x32_bf16 v[76:79], v[116:119], v[56:59], v[76:79]
	ds_read_b128 v[116:119], v164 offset:8192
	s_waitcnt lgkmcnt(3)
	v_mfma_f32_16x16x32_bf16 v[80:83], v[120:123], v[24:27], v[80:83]
	v_mfma_f32_16x16x32_bf16 v[84:87], v[120:123], v[56:59], v[84:87]
	ds_read_b128 v[120:123], v164 offset:16384
	s_waitcnt lgkmcnt(3)
	v_mfma_f32_16x16x32_bf16 v[88:91], v[124:127], v[24:27], v[88:91]
	v_mfma_f32_16x16x32_bf16 v[92:95], v[124:127], v[56:59], v[92:95]
	ds_read_b128 v[124:127], v164 offset:24576
	s_waitcnt lgkmcnt(3)
	v_mfma_f32_16x16x32_bf16 v[64:67], v[112:115], v[28:31], v[64:67]
	v_mfma_f32_16x16x32_bf16 v[68:71], v[112:115], v[60:63], v[68:71]
	s_waitcnt lgkmcnt(2)
	v_mfma_f32_16x16x32_bf16 v[72:75], v[116:119], v[28:31], v[72:75]
	v_mfma_f32_16x16x32_bf16 v[76:79], v[116:119], v[60:63], v[76:79]
	s_waitcnt lgkmcnt(1)
	v_mfma_f32_16x16x32_bf16 v[80:83], v[120:123], v[28:31], v[80:83]
	v_mfma_f32_16x16x32_bf16 v[84:87], v[120:123], v[60:63], v[84:87]
	s_waitcnt lgkmcnt(0)
	v_mfma_f32_16x16x32_bf16 v[88:91], v[124:127], v[28:31], v[88:91]
	v_mfma_f32_16x16x32_bf16 v[92:95], v[124:127], v[60:63], v[92:95]
.Lmylru_p0_0:
	s_cmp_eq_u32 s14, 0
	s_cbranch_scc0 .Lmylru_nm_1
	v_mov_b32_e32 v163, v162
	ds_read_b128 v[96:99], v163
	ds_read_b128 v[100:103], v163 offset:8192
	ds_read_b128 v[104:107], v163 offset:16384
	ds_read_b128 v[108:111], v163 offset:24576
	v_xor_b32_e32 v164, 0x40, v163
	ds_read_b128 v[112:115], v164
	ds_read_b128 v[116:119], v164 offset:8192
	ds_read_b128 v[120:123], v164 offset:16384
	ds_read_b128 v[124:127], v164 offset:24576
	s_waitcnt lgkmcnt(7)
	v_mfma_f32_16x16x32_bf16 v[64:67], v[96:99], v[0:3], 0
	v_mfma_f32_16x16x32_bf16 v[68:71], v[96:99], v[32:35], 0
	v_xor_b32_e32 v164, 0x80, v163
	ds_read_b128 v[96:99], v164
	s_waitcnt lgkmcnt(7)
	v_mfma_f32_16x16x32_bf16 v[72:75], v[100:103], v[0:3], 0
	v_mfma_f32_16x16x32_bf16 v[76:79], v[100:103], v[32:35], 0
	ds_read_b128 v[100:103], v164 offset:8192
	s_waitcnt lgkmcnt(7)
	v_mfma_f32_16x16x32_bf16 v[80:83], v[104:107], v[0:3], 0
	v_mfma_f32_16x16x32_bf16 v[84:87], v[104:107], v[32:35], 0
	ds_read_b128 v[104:107], v164 offset:16384
	s_waitcnt lgkmcnt(7)
	v_mfma_f32_16x16x32_bf16 v[88:91], v[108:111], v[0:3], 0
	v_mfma_f32_16x16x32_bf16 v[92:95], v[108:111], v[32:35], 0
	ds_read_b128 v[108:111], v164 offset:24576
	s_waitcnt lgkmcnt(7)
	v_mfma_f32_16x16x32_bf16 v[64:67], v[112:115], v[4:7], v[64:67]
	v_mfma_f32_16x16x32_bf16 v[68:71], v[112:115], v[36:39], v[68:71]
	v_xor_b32_e32 v164, 0xc0, v163
	ds_read_b128 v[112:115], v164
	s_waitcnt lgkmcnt(7)
	v_mfma_f32_16x16x32_bf16 v[72:75], v[116:119], v[4:7], v[72:75]
	v_mfma_f32_16x16x32_bf16 v[76:79], v[116:119], v[36:39], v[76:79]
	ds_read_b128 v[116:119], v164 offset:8192
	s_waitcnt lgkmcnt(7)
	v_mfma_f32_16x16x32_bf16 v[80:83], v[120:123], v[4:7], v[80:83]
	v_mfma_f32_16x16x32_bf16 v[84:87], v[120:123], v[36:39], v[84:87]
	ds_read_b128 v[120:123], v164 offset:16384
	s_waitcnt lgkmcnt(7)
	v_mfma_f32_16x16x32_bf16 v[88:91], v[124:127], v[4:7], v[88:91]
	v_mfma_f32_16x16x32_bf16 v[92:95], v[124:127], v[36:39], v[92:95]
	ds_read_b128 v[124:127], v164 offset:24576
	s_waitcnt lgkmcnt(7)
	v_mfma_f32_16x16x32_bf16 v[64:67], v[96:99], v[8:11], v[64:67]
	v_mfma_f32_16x16x32_bf16 v[68:71], v[96:99], v[40:43], v[68:71]
	v_xor_b32_e32 v164, 0x100, v163
	ds_read_b128 v[96:99], v164
	s_waitcnt lgkmcnt(7)
	v_mfma_f32_16x16x32_bf16 v[72:75], v[100:103], v[8:11], v[72:75]
	v_mfma_f32_16x16x32_bf16 v[76:79], v[100:103], v[40:43], v[76:79]
	ds_read_b128 v[100:103], v164 offset:8192
	s_waitcnt lgkmcnt(7)
	v_mfma_f32_16x16x32_bf16 v[80:83], v[104:107], v[8:11], v[80:83]
	v_mfma_f32_16x16x32_bf16 v[84:87], v[104:107], v[40:43], v[84:87]
	ds_read_b128 v[104:107], v164 offset:16384
	s_waitcnt lgkmcnt(7)
	v_mfma_f32_16x16x32_bf16 v[88:91], v[108:111], v[8:11], v[88:91]
	v_mfma_f32_16x16x32_bf16 v[92:95], v[108:111], v[40:43], v[92:95]
	ds_read_b128 v[108:111], v164 offset:24576
	s_waitcnt lgkmcnt(7)
	v_mfma_f32_16x16x32_bf16 v[64:67], v[112:115], v[12:15], v[64:67]
	v_mfma_f32_16x16x32_bf16 v[68:71], v[112:115], v[44:47], v[68:71]
	v_xor_b32_e32 v164, 0x140, v163
	ds_read_b128 v[112:115], v164
	s_waitcnt lgkmcnt(7)
	v_mfma_f32_16x16x32_bf16 v[72:75], v[116:119], v[12:15], v[72:75]
	v_mfma_f32_16x16x32_bf16 v[76:79], v[116:119], v[44:47], v[76:79]
	ds_read_b128 v[116:119], v164 offset:8192
	s_waitcnt lgkmcnt(7)
	v_mfma_f32_16x16x32_bf16 v[80:83], v[120:123], v[12:15], v[80:83]
	v_mfma_f32_16x16x32_bf16 v[84:87], v[120:123], v[44:47], v[84:87]
	ds_read_b128 v[120:123], v164 offset:16384
	s_waitcnt lgkmcnt(7)
	v_mfma_f32_16x16x32_bf16 v[88:91], v[124:127], v[12:15], v[88:91]
	v_mfma_f32_16x16x32_bf16 v[92:95], v[124:127], v[44:47], v[92:95]
	ds_read_b128 v[124:127], v164 offset:24576
	s_waitcnt lgkmcnt(7)
	v_mfma_f32_16x16x32_bf16 v[64:67], v[96:99], v[16:19], v[64:67]
	v_mfma_f32_16x16x32_bf16 v[68:71], v[96:99], v[48:51], v[68:71]
	v_xor_b32_e32 v164, 0x180, v163
	ds_read_b128 v[96:99], v164
	s_waitcnt lgkmcnt(7)
	v_mfma_f32_16x16x32_bf16 v[72:75], v[100:103], v[16:19], v[72:75]
	v_mfma_f32_16x16x32_bf16 v[76:79], v[100:103], v[48:51], v[76:79]
	ds_read_b128 v[100:103], v164 offset:8192
	s_waitcnt lgkmcnt(7)
	v_mfma_f32_16x16x32_bf16 v[80:83], v[104:107], v[16:19], v[80:83]
	v_mfma_f32_16x16x32_bf16 v[84:87], v[104:107], v[48:51], v[84:87]
	ds_read_b128 v[104:107], v164 offset:16384
	s_waitcnt lgkmcnt(7)
	v_mfma_f32_16x16x32_bf16 v[88:91], v[108:111], v[16:19], v[88:91]
	v_mfma_f32_16x16x32_bf16 v[92:95], v[108:111], v[48:51], v[92:95]
	ds_read_b128 v[108:111], v164 offset:24576
	s_waitcnt lgkmcnt(7)
	v_mfma_f32_16x16x32_bf16 v[64:67], v[112:115], v[20:23], v[64:67]
	v_mfma_f32_16x16x32_bf16 v[68:71], v[112:115], v[52:55], v[68:71]
	v_xor_b32_e32 v164, 0x1c0, v163
	ds_read_b128 v[112:115], v164
	s_waitcnt lgkmcnt(7)
	v_mfma_f32_16x16x32_bf16 v[72:75], v[116:119], v[20:23], v[72:75]
	v_mfma_f32_16x16x32_bf16 v[76:79], v[116:119], v[52:55], v[76:79]
	ds_read_b128 v[116:119], v164 offset:8192
	s_waitcnt lgkmcnt(7)
	v_mfma_f32_16x16x32_bf16 v[80:83], v[120:123], v[20:23], v[80:83]
	v_mfma_f32_16x16x32_bf16 v[84:87], v[120:123], v[52:55], v[84:87]
	ds_read_b128 v[120:123], v164 offset:16384
	s_waitcnt lgkmcnt(7)
	v_mfma_f32_16x16x32_bf16 v[88:91], v[124:127], v[20:23], v[88:91]
	v_mfma_f32_16x16x32_bf16 v[92:95], v[124:127], v[52:55], v[92:95]
	ds_read_b128 v[124:127], v164 offset:24576
	s_waitcnt lgkmcnt(7)
	v_mfma_f32_16x16x32_bf16 v[64:67], v[96:99], v[24:27], v[64:67]
	v_mfma_f32_16x16x32_bf16 v[68:71], v[96:99], v[56:59], v[68:71]
	s_waitcnt lgkmcnt(6)
	v_mfma_f32_16x16x32_bf16 v[72:75], v[100:103], v[24:27], v[72:75]
	v_mfma_f32_16x16x32_bf16 v[76:79], v[100:103], v[56:59], v[76:79]
	s_waitcnt lgkmcnt(5)
	v_mfma_f32_16x16x32_bf16 v[80:83], v[104:107], v[24:27], v[80:83]
	v_mfma_f32_16x16x32_bf16 v[84:87], v[104:107], v[56:59], v[84:87]
	s_waitcnt lgkmcnt(4)
	v_mfma_f32_16x16x32_bf16 v[88:91], v[108:111], v[24:27], v[88:91]
	v_mfma_f32_16x16x32_bf16 v[92:95], v[108:111], v[56:59], v[92:95]
	s_waitcnt lgkmcnt(3)
	v_mfma_f32_16x16x32_bf16 v[64:67], v[112:115], v[28:31], v[64:67]
	v_mfma_f32_16x16x32_bf16 v[68:71], v[112:115], v[60:63], v[68:71]
	s_waitcnt lgkmcnt(2)
	v_mfma_f32_16x16x32_bf16 v[72:75], v[116:119], v[28:31], v[72:75]
	v_mfma_f32_16x16x32_bf16 v[76:79], v[116:119], v[60:63], v[76:79]
	s_waitcnt lgkmcnt(1)
	v_mfma_f32_16x16x32_bf16 v[80:83], v[120:123], v[28:31], v[80:83]
	v_mfma_f32_16x16x32_bf16 v[84:87], v[120:123], v[60:63], v[84:87]
	s_waitcnt lgkmcnt(0)
	v_mfma_f32_16x16x32_bf16 v[88:91], v[124:127], v[28:31], v[88:91]
	v_mfma_f32_16x16x32_bf16 v[92:95], v[124:127], v[60:63], v[92:95]

.Lmylru_nodma_1:
	s_cmp_eq_u32 s14, 0
	s_cbranch_scc1 .Lmylru_ne_1
	s_cmp_eq_u32 s13, 17
	s_cbranch_scc1 .Lmylru_ne_1
	v_or_b32_e32 v163, 0x10000, v162
	ds_read_b128 v[112:115], v163
	ds_read_b128 v[116:119], v163 offset:8192
	ds_read_b128 v[120:123], v163 offset:16384
	ds_read_b128 v[124:127], v163 offset:24576
	s_waitcnt lgkmcnt(3)
	v_mfma_f32_16x16x32_bf16 v[64:67], v[112:115], v[0:3], 0
	v_mfma_f32_16x16x32_bf16 v[68:71], v[112:115], v[32:35], 0
	v_xor_b32_e32 v164, 0x40, v163
	ds_read_b128 v[112:115], v164
	s_waitcnt lgkmcnt(3)
	v_mfma_f32_16x16x32_bf16 v[72:75], v[116:119], v[0:3], 0
	v_mfma_f32_16x16x32_bf16 v[76:79], v[116:119], v[32:35], 0
	ds_read_b128 v[116:119], v164 offset:8192
	s_waitcnt lgkmcnt(3)
	v_mfma_f32_16x16x32_bf16 v[80:83], v[120:123], v[0:3], 0
	v_mfma_f32_16x16x32_bf16 v[84:87], v[120:123], v[32:35], 0
	ds_read_b128 v[120:123], v164 offset:16384
	s_waitcnt lgkmcnt(3)
	v_mfma_f32_16x16x32_bf16 v[88:91], v[124:127], v[0:3], 0
	v_mfma_f32_16x16x32_bf16 v[92:95], v[124:127], v[32:35], 0
	ds_read_b128 v[124:127], v164 offset:24576
	s_waitcnt lgkmcnt(3)
	v_mfma_f32_16x16x32_bf16 v[64:67], v[112:115], v[4:7], v[64:67]
	v_mfma_f32_16x16x32_bf16 v[68:71], v[112:115], v[36:39], v[68:71]
	v_xor_b32_e32 v164, 0x80, v163
	ds_read_b128 v[112:115], v164
	s_waitcnt lgkmcnt(3)
	v_mfma_f32_16x16x32_bf16 v[72:75], v[116:119], v[4:7], v[72:75]
	v_mfma_f32_16x16x32_bf16 v[76:79], v[116:119], v[36:39], v[76:79]
	ds_read_b128 v[116:119], v164 offset:8192
	s_waitcnt lgkmcnt(3)
	v_mfma_f32_16x16x32_bf16 v[80:83], v[120:123], v[4:7], v[80:83]
	v_mfma_f32_16x16x32_bf16 v[84:87], v[120:123], v[36:39], v[84:87]
	ds_read_b128 v[120:123], v164 offset:16384
	s_waitcnt lgkmcnt(3)
	v_mfma_f32_16x16x32_bf16 v[88:91], v[124:127], v[4:7], v[88:91]
	v_mfma_f32_16x16x32_bf16 v[92:95], v[124:127], v[36:39], v[92:95]
	ds_read_b128 v[124:127], v164 offset:24576
	s_waitcnt lgkmcnt(3)
	v_mfma_f32_16x16x32_bf16 v[64:67], v[112:115], v[8:11], v[64:67]
	v_mfma_f32_16x16x32_bf16 v[68:71], v[112:115], v[40:43], v[68:71]
	v_xor_b32_e32 v164, 0xc0, v163
	ds_read_b128 v[112:115], v164
	s_waitcnt lgkmcnt(3)
	v_mfma_f32_16x16x32_bf16 v[72:75], v[116:119], v[8:11], v[72:75]
	v_mfma_f32_16x16x32_bf16 v[76:79], v[116:119], v[40:43], v[76:79]
	ds_read_b128 v[116:119], v164 offset:8192
	s_waitcnt lgkmcnt(3)
	v_mfma_f32_16x16x32_bf16 v[80:83], v[120:123], v[8:11], v[80:83]
	v_mfma_f32_16x16x32_bf16 v[84:87], v[120:123], v[40:43], v[84:87]
	ds_read_b128 v[120:123], v164 offset:16384
	s_waitcnt lgkmcnt(3)
	v_mfma_f32_16x16x32_bf16 v[88:91], v[124:127], v[8:11], v[88:91]
	v_mfma_f32_16x16x32_bf16 v[92:95], v[124:127], v[40:43], v[92:95]
	ds_read_b128 v[124:127], v164 offset:24576
	s_waitcnt lgkmcnt(3)
	v_mfma_f32_16x16x32_bf16 v[64:67], v[112:115], v[12:15], v[64:67]
	v_mfma_f32_16x16x32_bf16 v[68:71], v[112:115], v[44:47], v[68:71]
	v_xor_b32_e32 v164, 0x100, v163
	ds_read_b128 v[112:115], v164
	s_waitcnt lgkmcnt(3)
	v_mfma_f32_16x16x32_bf16 v[72:75], v[116:119], v[12:15], v[72:75]
	v_mfma_f32_16x16x32_bf16 v[76:79], v[116:119], v[44:47], v[76:79]
	ds_read_b128 v[116:119], v164 offset:8192
	s_waitcnt lgkmcnt(3)
	v_mfma_f32_16x16x32_bf16 v[80:83], v[120:123], v[12:15], v[80:83]
	v_mfma_f32_16x16x32_bf16 v[84:87], v[120:123], v[44:47], v[84:87]
	ds_read_b128 v[120:123], v164 offset:16384
	s_waitcnt lgkmcnt(3)
	v_mfma_f32_16x16x32_bf16 v[88:91], v[124:127], v[12:15], v[88:91]
	v_mfma_f32_16x16x32_bf16 v[92:95], v[124:127], v[44:47], v[92:95]
	ds_read_b128 v[124:127], v164 offset:24576
	s_waitcnt lgkmcnt(3)
	v_mfma_f32_16x16x32_bf16 v[64:67], v[112:115], v[16:19], v[64:67]
	v_mfma_f32_16x16x32_bf16 v[68:71], v[112:115], v[48:51], v[68:71]
	v_xor_b32_e32 v164, 0x140, v163
	ds_read_b128 v[112:115], v164
	s_waitcnt lgkmcnt(3)
	v_mfma_f32_16x16x32_bf16 v[72:75], v[116:119], v[16:19], v[72:75]
	v_mfma_f32_16x16x32_bf16 v[76:79], v[116:119], v[48:51], v[76:79]
	ds_read_b128 v[116:119], v164 offset:8192
	s_waitcnt lgkmcnt(3)
	v_mfma_f32_16x16x32_bf16 v[80:83], v[120:123], v[16:19], v[80:83]
	v_mfma_f32_16x16x32_bf16 v[84:87], v[120:123], v[48:51], v[84:87]
	ds_read_b128 v[120:123], v164 offset:16384
	s_waitcnt lgkmcnt(3)
	v_mfma_f32_16x16x32_bf16 v[88:91], v[124:127], v[16:19], v[88:91]
	v_mfma_f32_16x16x32_bf16 v[92:95], v[124:127], v[48:51], v[92:95]
	ds_read_b128 v[124:127], v164 offset:24576
	s_waitcnt lgkmcnt(3)
	v_mfma_f32_16x16x32_bf16 v[64:67], v[112:115], v[20:23], v[64:67]
	v_mfma_f32_16x16x32_bf16 v[68:71], v[112:115], v[52:55], v[68:71]
	v_xor_b32_e32 v164, 0x180, v163
	ds_read_b128 v[112:115], v164
	s_waitcnt lgkmcnt(3)
	v_mfma_f32_16x16x32_bf16 v[72:75], v[116:119], v[20:23], v[72:75]
	v_mfma_f32_16x16x32_bf16 v[76:79], v[116:119], v[52:55], v[76:79]
	ds_read_b128 v[116:119], v164 offset:8192
	s_waitcnt lgkmcnt(3)
	v_mfma_f32_16x16x32_bf16 v[80:83], v[120:123], v[20:23], v[80:83]
	v_mfma_f32_16x16x32_bf16 v[84:87], v[120:123], v[52:55], v[84:87]
	ds_read_b128 v[120:123], v164 offset:16384
	s_waitcnt lgkmcnt(3)
	v_mfma_f32_16x16x32_bf16 v[88:91], v[124:127], v[20:23], v[88:91]
	v_mfma_f32_16x16x32_bf16 v[92:95], v[124:127], v[52:55], v[92:95]
	ds_read_b128 v[124:127], v164 offset:24576
	s_waitcnt lgkmcnt(3)
	v_mfma_f32_16x16x32_bf16 v[64:67], v[112:115], v[24:27], v[64:67]
	v_mfma_f32_16x16x32_bf16 v[68:71], v[112:115], v[56:59], v[68:71]
	v_xor_b32_e32 v164, 0x1c0, v163
	ds_read_b128 v[112:115], v164
	s_waitcnt lgkmcnt(3)
	v_mfma_f32_16x16x32_bf16 v[72:75], v[116:119], v[24:27], v[72:75]
	v_mfma_f32_16x16x32_bf16 v[76:79], v[116:119], v[56:59], v[76:79]
	ds_read_b128 v[116:119], v164 offset:8192
	s_waitcnt lgkmcnt(3)
	v_mfma_f32_16x16x32_bf16 v[80:83], v[120:123], v[24:27], v[80:83]
	v_mfma_f32_16x16x32_bf16 v[84:87], v[120:123], v[56:59], v[84:87]
	ds_read_b128 v[120:123], v164 offset:16384
	s_waitcnt lgkmcnt(3)
	v_mfma_f32_16x16x32_bf16 v[88:91], v[124:127], v[24:27], v[88:91]
	v_mfma_f32_16x16x32_bf16 v[92:95], v[124:127], v[56:59], v[92:95]
	ds_read_b128 v[124:127], v164 offset:24576
	s_waitcnt lgkmcnt(3)
	v_mfma_f32_16x16x32_bf16 v[64:67], v[112:115], v[28:31], v[64:67]
	v_mfma_f32_16x16x32_bf16 v[68:71], v[112:115], v[60:63], v[68:71]
	s_waitcnt lgkmcnt(2)
	v_mfma_f32_16x16x32_bf16 v[72:75], v[116:119], v[28:31], v[72:75]
	v_mfma_f32_16x16x32_bf16 v[76:79], v[116:119], v[60:63], v[76:79]
	s_waitcnt lgkmcnt(1)
	v_mfma_f32_16x16x32_bf16 v[80:83], v[120:123], v[28:31], v[80:83]
	v_mfma_f32_16x16x32_bf16 v[84:87], v[120:123], v[60:63], v[84:87]
	s_waitcnt lgkmcnt(0)
	v_mfma_f32_16x16x32_bf16 v[88:91], v[124:127], v[28:31], v[88:91]
	v_mfma_f32_16x16x32_bf16 v[92:95], v[124:127], v[60:63], v[92:95]
.Lmylru_ne_1:
	ds_read_b64 v[178:179], v208
	ds_read_b64 v[180:181], v208 offset:512
	s_waitcnt lgkmcnt(0)
	v_fma_f32 v182, v176, v178, v179
	v_cndmask_b32_e64 v183, v176, v182, s[38:39]
	v_fma_f32 v176, v182, v180, v181
	s_add_i32 s13, s13, 1
	s_cmp_eq_u32 s14, 0
	s_cbranch_scc0 .Lmylru_nm_2
	v_or_b32_e32 v163, 0x10000, v162
	ds_read_b128 v[96:99], v163
	ds_read_b128 v[100:103], v163 offset:8192
	ds_read_b128 v[104:107], v163 offset:16384
	ds_read_b128 v[108:111], v163 offset:24576
	v_xor_b32_e32 v164, 0x40, v163
	ds_read_b128 v[112:115], v164
	ds_read_b128 v[116:119], v164 offset:8192
	ds_read_b128 v[120:123], v164 offset:16384
	ds_read_b128 v[124:127], v164 offset:24576
	s_waitcnt lgkmcnt(7)
	v_mfma_f32_16x16x32_bf16 v[64:67], v[96:99], v[0:3], 0
	v_mfma_f32_16x16x32_bf16 v[68:71], v[96:99], v[32:35], 0
	v_xor_b32_e32 v164, 0x80, v163
	ds_read_b128 v[96:99], v164
	s_waitcnt lgkmcnt(7)
	v_mfma_f32_16x16x32_bf16 v[72:75], v[100:103], v[0:3], 0
	v_mfma_f32_16x16x32_bf16 v[76:79], v[100:103], v[32:35], 0
	ds_read_b128 v[100:103], v164 offset:8192
	s_waitcnt lgkmcnt(7)
	v_mfma_f32_16x16x32_bf16 v[80:83], v[104:107], v[0:3], 0
	v_mfma_f32_16x16x32_bf16 v[84:87], v[104:107], v[32:35], 0
	ds_read_b128 v[104:107], v164 offset:16384
	s_waitcnt lgkmcnt(7)
	v_mfma_f32_16x16x32_bf16 v[88:91], v[108:111], v[0:3], 0
	v_mfma_f32_16x16x32_bf16 v[92:95], v[108:111], v[32:35], 0
	ds_read_b128 v[108:111], v164 offset:24576
	s_waitcnt lgkmcnt(7)
	v_mfma_f32_16x16x32_bf16 v[64:67], v[112:115], v[4:7], v[64:67]
	v_mfma_f32_16x16x32_bf16 v[68:71], v[112:115], v[36:39], v[68:71]
	v_xor_b32_e32 v164, 0xc0, v163
	ds_read_b128 v[112:115], v164
	s_waitcnt lgkmcnt(7)
	v_mfma_f32_16x16x32_bf16 v[72:75], v[116:119], v[4:7], v[72:75]
	v_mfma_f32_16x16x32_bf16 v[76:79], v[116:119], v[36:39], v[76:79]
	ds_read_b128 v[116:119], v164 offset:8192
	s_waitcnt lgkmcnt(7)
	v_mfma_f32_16x16x32_bf16 v[80:83], v[120:123], v[4:7], v[80:83]
	v_mfma_f32_16x16x32_bf16 v[84:87], v[120:123], v[36:39], v[84:87]
	ds_read_b128 v[120:123], v164 offset:16384
	s_waitcnt lgkmcnt(7)
	v_mfma_f32_16x16x32_bf16 v[88:91], v[124:127], v[4:7], v[88:91]
	v_mfma_f32_16x16x32_bf16 v[92:95], v[124:127], v[36:39], v[92:95]
	ds_read_b128 v[124:127], v164 offset:24576
	s_waitcnt lgkmcnt(7)
	v_mfma_f32_16x16x32_bf16 v[64:67], v[96:99], v[8:11], v[64:67]
	v_mfma_f32_16x16x32_bf16 v[68:71], v[96:99], v[40:43], v[68:71]
	v_xor_b32_e32 v164, 0x100, v163
	ds_read_b128 v[96:99], v164
	s_waitcnt lgkmcnt(7)
	v_mfma_f32_16x16x32_bf16 v[72:75], v[100:103], v[8:11], v[72:75]
	v_mfma_f32_16x16x32_bf16 v[76:79], v[100:103], v[40:43], v[76:79]
	ds_read_b128 v[100:103], v164 offset:8192
	s_waitcnt lgkmcnt(7)
	v_mfma_f32_16x16x32_bf16 v[80:83], v[104:107], v[8:11], v[80:83]
	v_mfma_f32_16x16x32_bf16 v[84:87], v[104:107], v[40:43], v[84:87]
	ds_read_b128 v[104:107], v164 offset:16384
	s_waitcnt lgkmcnt(7)
	v_mfma_f32_16x16x32_bf16 v[88:91], v[108:111], v[8:11], v[88:91]
	v_mfma_f32_16x16x32_bf16 v[92:95], v[108:111], v[40:43], v[92:95]
	ds_read_b128 v[108:111], v164 offset:24576
	s_waitcnt lgkmcnt(7)
	v_mfma_f32_16x16x32_bf16 v[64:67], v[112:115], v[12:15], v[64:67]
	v_mfma_f32_16x16x32_bf16 v[68:71], v[112:115], v[44:47], v[68:71]
	v_xor_b32_e32 v164, 0x140, v163
	ds_read_b128 v[112:115], v164
	s_waitcnt lgkmcnt(7)
	v_mfma_f32_16x16x32_bf16 v[72:75], v[116:119], v[12:15], v[72:75]
	v_mfma_f32_16x16x32_bf16 v[76:79], v[116:119], v[44:47], v[76:79]
	ds_read_b128 v[116:119], v164 offset:8192
	s_waitcnt lgkmcnt(7)
	v_mfma_f32_16x16x32_bf16 v[80:83], v[120:123], v[12:15], v[80:83]
	v_mfma_f32_16x16x32_bf16 v[84:87], v[120:123], v[44:47], v[84:87]
	ds_read_b128 v[120:123], v164 offset:16384
	s_waitcnt lgkmcnt(7)
	v_mfma_f32_16x16x32_bf16 v[88:91], v[124:127], v[12:15], v[88:91]
	v_mfma_f32_16x16x32_bf16 v[92:95], v[124:127], v[44:47], v[92:95]
	ds_read_b128 v[124:127], v164 offset:24576
	s_waitcnt lgkmcnt(7)
	v_mfma_f32_16x16x32_bf16 v[64:67], v[96:99], v[16:19], v[64:67]
	v_mfma_f32_16x16x32_bf16 v[68:71], v[96:99], v[48:51], v[68:71]
	v_xor_b32_e32 v164, 0x180, v163
	ds_read_b128 v[96:99], v164
	s_waitcnt lgkmcnt(7)
	v_mfma_f32_16x16x32_bf16 v[72:75], v[100:103], v[16:19], v[72:75]
	v_mfma_f32_16x16x32_bf16 v[76:79], v[100:103], v[48:51], v[76:79]
	ds_read_b128 v[100:103], v164 offset:8192
	s_waitcnt lgkmcnt(7)
	v_mfma_f32_16x16x32_bf16 v[80:83], v[104:107], v[16:19], v[80:83]
	v_mfma_f32_16x16x32_bf16 v[84:87], v[104:107], v[48:51], v[84:87]
	ds_read_b128 v[104:107], v164 offset:16384
	s_waitcnt lgkmcnt(7)
	v_mfma_f32_16x16x32_bf16 v[88:91], v[108:111], v[16:19], v[88:91]
	v_mfma_f32_16x16x32_bf16 v[92:95], v[108:111], v[48:51], v[92:95]
	ds_read_b128 v[108:111], v164 offset:24576
	s_waitcnt lgkmcnt(7)
	v_mfma_f32_16x16x32_bf16 v[64:67], v[112:115], v[20:23], v[64:67]
	v_mfma_f32_16x16x32_bf16 v[68:71], v[112:115], v[52:55], v[68:71]
	v_xor_b32_e32 v164, 0x1c0, v163
	ds_read_b128 v[112:115], v164
	s_waitcnt lgkmcnt(7)
	v_mfma_f32_16x16x32_bf16 v[72:75], v[116:119], v[20:23], v[72:75]
	v_mfma_f32_16x16x32_bf16 v[76:79], v[116:119], v[52:55], v[76:79]
	ds_read_b128 v[116:119], v164 offset:8192
	s_waitcnt lgkmcnt(7)
	v_mfma_f32_16x16x32_bf16 v[80:83], v[120:123], v[20:23], v[80:83]
	v_mfma_f32_16x16x32_bf16 v[84:87], v[120:123], v[52:55], v[84:87]
	ds_read_b128 v[120:123], v164 offset:16384
	s_waitcnt lgkmcnt(7)
	v_mfma_f32_16x16x32_bf16 v[88:91], v[124:127], v[20:23], v[88:91]
	v_mfma_f32_16x16x32_bf16 v[92:95], v[124:127], v[52:55], v[92:95]
	ds_read_b128 v[124:127], v164 offset:24576
	s_waitcnt lgkmcnt(7)
	v_mfma_f32_16x16x32_bf16 v[64:67], v[96:99], v[24:27], v[64:67]
	v_mfma_f32_16x16x32_bf16 v[68:71], v[96:99], v[56:59], v[68:71]
	s_waitcnt lgkmcnt(6)
	v_mfma_f32_16x16x32_bf16 v[72:75], v[100:103], v[24:27], v[72:75]
	v_mfma_f32_16x16x32_bf16 v[76:79], v[100:103], v[56:59], v[76:79]
	s_waitcnt lgkmcnt(5)
	v_mfma_f32_16x16x32_bf16 v[80:83], v[104:107], v[24:27], v[80:83]
	v_mfma_f32_16x16x32_bf16 v[84:87], v[104:107], v[56:59], v[84:87]
	s_waitcnt lgkmcnt(4)
	v_mfma_f32_16x16x32_bf16 v[88:91], v[108:111], v[24:27], v[88:91]
	v_mfma_f32_16x16x32_bf16 v[92:95], v[108:111], v[56:59], v[92:95]
	s_waitcnt lgkmcnt(3)
	v_mfma_f32_16x16x32_bf16 v[64:67], v[112:115], v[28:31], v[64:67]
	v_mfma_f32_16x16x32_bf16 v[68:71], v[112:115], v[60:63], v[68:71]
	s_waitcnt lgkmcnt(2)
	v_mfma_f32_16x16x32_bf16 v[72:75], v[116:119], v[28:31], v[72:75]
	v_mfma_f32_16x16x32_bf16 v[76:79], v[116:119], v[60:63], v[76:79]
	s_waitcnt lgkmcnt(1)
	v_mfma_f32_16x16x32_bf16 v[80:83], v[120:123], v[28:31], v[80:83]
	v_mfma_f32_16x16x32_bf16 v[84:87], v[120:123], v[60:63], v[84:87]
	s_waitcnt lgkmcnt(0)
	v_mfma_f32_16x16x32_bf16 v[88:91], v[124:127], v[28:31], v[88:91]
	v_mfma_f32_16x16x32_bf16 v[92:95], v[124:127], v[60:63], v[92:95]

.Lmylru_nodma_2:
	s_cmp_eq_u32 s14, 0
	s_cbranch_scc1 .Lmylru_ne_2
	s_cmp_eq_u32 s13, 17
	s_cbranch_scc1 .Lmylru_ne_2
	v_mov_b32_e32 v163, v162
	ds_read_b128 v[112:115], v163
	ds_read_b128 v[116:119], v163 offset:8192
	ds_read_b128 v[120:123], v163 offset:16384
	ds_read_b128 v[124:127], v163 offset:24576
	s_waitcnt lgkmcnt(3)
	v_mfma_f32_16x16x32_bf16 v[64:67], v[112:115], v[0:3], 0
	v_mfma_f32_16x16x32_bf16 v[68:71], v[112:115], v[32:35], 0
	v_xor_b32_e32 v164, 0x40, v163
	ds_read_b128 v[112:115], v164
	s_waitcnt lgkmcnt(3)
	v_mfma_f32_16x16x32_bf16 v[72:75], v[116:119], v[0:3], 0
	v_mfma_f32_16x16x32_bf16 v[76:79], v[116:119], v[32:35], 0
	ds_read_b128 v[116:119], v164 offset:8192
	s_waitcnt lgkmcnt(3)
	v_mfma_f32_16x16x32_bf16 v[80:83], v[120:123], v[0:3], 0
	v_mfma_f32_16x16x32_bf16 v[84:87], v[120:123], v[32:35], 0
	ds_read_b128 v[120:123], v164 offset:16384
	s_waitcnt lgkmcnt(3)
	v_mfma_f32_16x16x32_bf16 v[88:91], v[124:127], v[0:3], 0
	v_mfma_f32_16x16x32_bf16 v[92:95], v[124:127], v[32:35], 0
	ds_read_b128 v[124:127], v164 offset:24576
	s_waitcnt lgkmcnt(3)
	v_mfma_f32_16x16x32_bf16 v[64:67], v[112:115], v[4:7], v[64:67]
	v_mfma_f32_16x16x32_bf16 v[68:71], v[112:115], v[36:39], v[68:71]
	v_xor_b32_e32 v164, 0x80, v163
	ds_read_b128 v[112:115], v164
	s_waitcnt lgkmcnt(3)
	v_mfma_f32_16x16x32_bf16 v[72:75], v[116:119], v[4:7], v[72:75]
	v_mfma_f32_16x16x32_bf16 v[76:79], v[116:119], v[36:39], v[76:79]
	ds_read_b128 v[116:119], v164 offset:8192
	s_waitcnt lgkmcnt(3)
	v_mfma_f32_16x16x32_bf16 v[80:83], v[120:123], v[4:7], v[80:83]
	v_mfma_f32_16x16x32_bf16 v[84:87], v[120:123], v[36:39], v[84:87]
	ds_read_b128 v[120:123], v164 offset:16384
	s_waitcnt lgkmcnt(3)
	v_mfma_f32_16x16x32_bf16 v[88:91], v[124:127], v[4:7], v[88:91]
	v_mfma_f32_16x16x32_bf16 v[92:95], v[124:127], v[36:39], v[92:95]
	ds_read_b128 v[124:127], v164 offset:24576
	s_waitcnt lgkmcnt(3)
	v_mfma_f32_16x16x32_bf16 v[64:67], v[112:115], v[8:11], v[64:67]
	v_mfma_f32_16x16x32_bf16 v[68:71], v[112:115], v[40:43], v[68:71]
	v_xor_b32_e32 v164, 0xc0, v163
	ds_read_b128 v[112:115], v164
	s_waitcnt lgkmcnt(3)
	v_mfma_f32_16x16x32_bf16 v[72:75], v[116:119], v[8:11], v[72:75]
	v_mfma_f32_16x16x32_bf16 v[76:79], v[116:119], v[40:43], v[76:79]
	ds_read_b128 v[116:119], v164 offset:8192
	s_waitcnt lgkmcnt(3)
	v_mfma_f32_16x16x32_bf16 v[80:83], v[120:123], v[8:11], v[80:83]
	v_mfma_f32_16x16x32_bf16 v[84:87], v[120:123], v[40:43], v[84:87]
	ds_read_b128 v[120:123], v164 offset:16384
	s_waitcnt lgkmcnt(3)
	v_mfma_f32_16x16x32_bf16 v[88:91], v[124:127], v[8:11], v[88:91]
	v_mfma_f32_16x16x32_bf16 v[92:95], v[124:127], v[40:43], v[92:95]
	ds_read_b128 v[124:127], v164 offset:24576
	s_waitcnt lgkmcnt(3)
	v_mfma_f32_16x16x32_bf16 v[64:67], v[112:115], v[12:15], v[64:67]
	v_mfma_f32_16x16x32_bf16 v[68:71], v[112:115], v[44:47], v[68:71]
	v_xor_b32_e32 v164, 0x100, v163
	ds_read_b128 v[112:115], v164
	s_waitcnt lgkmcnt(3)
	v_mfma_f32_16x16x32_bf16 v[72:75], v[116:119], v[12:15], v[72:75]
	v_mfma_f32_16x16x32_bf16 v[76:79], v[116:119], v[44:47], v[76:79]
	ds_read_b128 v[116:119], v164 offset:8192
	s_waitcnt lgkmcnt(3)
	v_mfma_f32_16x16x32_bf16 v[80:83], v[120:123], v[12:15], v[80:83]
	v_mfma_f32_16x16x32_bf16 v[84:87], v[120:123], v[44:47], v[84:87]
	ds_read_b128 v[120:123], v164 offset:16384
	s_waitcnt lgkmcnt(3)
	v_mfma_f32_16x16x32_bf16 v[88:91], v[124:127], v[12:15], v[88:91]
	v_mfma_f32_16x16x32_bf16 v[92:95], v[124:127], v[44:47], v[92:95]
	ds_read_b128 v[124:127], v164 offset:24576
	s_waitcnt lgkmcnt(3)
	v_mfma_f32_16x16x32_bf16 v[64:67], v[112:115], v[16:19], v[64:67]
	v_mfma_f32_16x16x32_bf16 v[68:71], v[112:115], v[48:51], v[68:71]
	v_xor_b32_e32 v164, 0x140, v163
	ds_read_b128 v[112:115], v164
	s_waitcnt lgkmcnt(3)
	v_mfma_f32_16x16x32_bf16 v[72:75], v[116:119], v[16:19], v[72:75]
	v_mfma_f32_16x16x32_bf16 v[76:79], v[116:119], v[48:51], v[76:79]
	ds_read_b128 v[116:119], v164 offset:8192
	s_waitcnt lgkmcnt(3)
	v_mfma_f32_16x16x32_bf16 v[80:83], v[120:123], v[16:19], v[80:83]
	v_mfma_f32_16x16x32_bf16 v[84:87], v[120:123], v[48:51], v[84:87]
	ds_read_b128 v[120:123], v164 offset:16384
	s_waitcnt lgkmcnt(3)
	v_mfma_f32_16x16x32_bf16 v[88:91], v[124:127], v[16:19], v[88:91]
	v_mfma_f32_16x16x32_bf16 v[92:95], v[124:127], v[48:51], v[92:95]
	ds_read_b128 v[124:127], v164 offset:24576
	s_waitcnt lgkmcnt(3)
	v_mfma_f32_16x16x32_bf16 v[64:67], v[112:115], v[20:23], v[64:67]
	v_mfma_f32_16x16x32_bf16 v[68:71], v[112:115], v[52:55], v[68:71]
	v_xor_b32_e32 v164, 0x180, v163
	ds_read_b128 v[112:115], v164
	s_waitcnt lgkmcnt(3)
	v_mfma_f32_16x16x32_bf16 v[72:75], v[116:119], v[20:23], v[72:75]
	v_mfma_f32_16x16x32_bf16 v[76:79], v[116:119], v[52:55], v[76:79]
	ds_read_b128 v[116:119], v164 offset:8192
	s_waitcnt lgkmcnt(3)
	v_mfma_f32_16x16x32_bf16 v[80:83], v[120:123], v[20:23], v[80:83]
	v_mfma_f32_16x16x32_bf16 v[84:87], v[120:123], v[52:55], v[84:87]
	ds_read_b128 v[120:123], v164 offset:16384
	s_waitcnt lgkmcnt(3)
	v_mfma_f32_16x16x32_bf16 v[88:91], v[124:127], v[20:23], v[88:91]
	v_mfma_f32_16x16x32_bf16 v[92:95], v[124:127], v[52:55], v[92:95]
	ds_read_b128 v[124:127], v164 offset:24576
	s_waitcnt lgkmcnt(3)
	v_mfma_f32_16x16x32_bf16 v[64:67], v[112:115], v[24:27], v[64:67]
	v_mfma_f32_16x16x32_bf16 v[68:71], v[112:115], v[56:59], v[68:71]
	v_xor_b32_e32 v164, 0x1c0, v163
	ds_read_b128 v[112:115], v164
	s_waitcnt lgkmcnt(3)
	v_mfma_f32_16x16x32_bf16 v[72:75], v[116:119], v[24:27], v[72:75]
	v_mfma_f32_16x16x32_bf16 v[76:79], v[116:119], v[56:59], v[76:79]
	ds_read_b128 v[116:119], v164 offset:8192
	s_waitcnt lgkmcnt(3)
	v_mfma_f32_16x16x32_bf16 v[80:83], v[120:123], v[24:27], v[80:83]
	v_mfma_f32_16x16x32_bf16 v[84:87], v[120:123], v[56:59], v[84:87]
	ds_read_b128 v[120:123], v164 offset:16384
	s_waitcnt lgkmcnt(3)
	v_mfma_f32_16x16x32_bf16 v[88:91], v[124:127], v[24:27], v[88:91]
	v_mfma_f32_16x16x32_bf16 v[92:95], v[124:127], v[56:59], v[92:95]
	ds_read_b128 v[124:127], v164 offset:24576
	s_waitcnt lgkmcnt(3)
	v_mfma_f32_16x16x32_bf16 v[64:67], v[112:115], v[28:31], v[64:67]
	v_mfma_f32_16x16x32_bf16 v[68:71], v[112:115], v[60:63], v[68:71]
	s_waitcnt lgkmcnt(2)
	v_mfma_f32_16x16x32_bf16 v[72:75], v[116:119], v[28:31], v[72:75]
	v_mfma_f32_16x16x32_bf16 v[76:79], v[116:119], v[60:63], v[76:79]
	s_waitcnt lgkmcnt(1)
	v_mfma_f32_16x16x32_bf16 v[80:83], v[120:123], v[28:31], v[80:83]
	v_mfma_f32_16x16x32_bf16 v[84:87], v[120:123], v[60:63], v[84:87]
	s_waitcnt lgkmcnt(0)
	v_mfma_f32_16x16x32_bf16 v[88:91], v[124:127], v[28:31], v[88:91]
	v_mfma_f32_16x16x32_bf16 v[92:95], v[124:127], v[60:63], v[92:95]

.Lmylru_loop_0:
	s_add_i32 s54, s13, -2
	s_lshl_b32 s55, s54, 14
	s_lshl_b32 s56, s6, 11
	s_add_i32 s55, s55, s56
	s_add_u32 s44, s22, s55
	s_addc_u32 s45, s23, 0
	s_cmp_eq_u32 s14, 0
	s_cbranch_scc0 .Lmylru_nm_3
	v_mov_b32_e32 v163, v162
	ds_read_b128 v[96:99], v163
	ds_read_b128 v[100:103], v163 offset:8192
	ds_read_b128 v[104:107], v163 offset:16384
	ds_read_b128 v[108:111], v163 offset:24576
	v_xor_b32_e32 v164, 0x40, v163
	ds_read_b128 v[112:115], v164
	ds_read_b128 v[116:119], v164 offset:8192
	ds_read_b128 v[120:123], v164 offset:16384
	ds_read_b128 v[124:127], v164 offset:24576
	s_waitcnt lgkmcnt(7)
	v_mfma_f32_16x16x32_bf16 v[64:67], v[96:99], v[0:3], 0
	v_mfma_f32_16x16x32_bf16 v[68:71], v[96:99], v[32:35], 0
	v_xor_b32_e32 v164, 0x80, v163
	ds_read_b128 v[96:99], v164
	s_waitcnt lgkmcnt(7)
	v_mfma_f32_16x16x32_bf16 v[72:75], v[100:103], v[0:3], 0
	v_mfma_f32_16x16x32_bf16 v[76:79], v[100:103], v[32:35], 0
	ds_read_b128 v[100:103], v164 offset:8192
	s_waitcnt lgkmcnt(7)
	v_mfma_f32_16x16x32_bf16 v[80:83], v[104:107], v[0:3], 0
	v_mfma_f32_16x16x32_bf16 v[84:87], v[104:107], v[32:35], 0
	ds_read_b128 v[104:107], v164 offset:16384
	s_waitcnt lgkmcnt(7)
	v_mfma_f32_16x16x32_bf16 v[88:91], v[108:111], v[0:3], 0
	v_mfma_f32_16x16x32_bf16 v[92:95], v[108:111], v[32:35], 0
	ds_read_b128 v[108:111], v164 offset:24576
	s_waitcnt lgkmcnt(7)
	v_mfma_f32_16x16x32_bf16 v[64:67], v[112:115], v[4:7], v[64:67]
	v_mfma_f32_16x16x32_bf16 v[68:71], v[112:115], v[36:39], v[68:71]
	v_xor_b32_e32 v164, 0xc0, v163
	ds_read_b128 v[112:115], v164
	s_waitcnt lgkmcnt(7)
	v_mfma_f32_16x16x32_bf16 v[72:75], v[116:119], v[4:7], v[72:75]
	v_mfma_f32_16x16x32_bf16 v[76:79], v[116:119], v[36:39], v[76:79]
	ds_read_b128 v[116:119], v164 offset:8192
	s_waitcnt lgkmcnt(7)
	v_mfma_f32_16x16x32_bf16 v[80:83], v[120:123], v[4:7], v[80:83]
	v_mfma_f32_16x16x32_bf16 v[84:87], v[120:123], v[36:39], v[84:87]
	ds_read_b128 v[120:123], v164 offset:16384
	s_waitcnt lgkmcnt(7)
	v_mfma_f32_16x16x32_bf16 v[88:91], v[124:127], v[4:7], v[88:91]
	v_mfma_f32_16x16x32_bf16 v[92:95], v[124:127], v[36:39], v[92:95]
	ds_read_b128 v[124:127], v164 offset:24576
	s_waitcnt lgkmcnt(7)
	v_mfma_f32_16x16x32_bf16 v[64:67], v[96:99], v[8:11], v[64:67]
	v_mfma_f32_16x16x32_bf16 v[68:71], v[96:99], v[40:43], v[68:71]
	v_xor_b32_e32 v164, 0x100, v163
	ds_read_b128 v[96:99], v164
	s_waitcnt lgkmcnt(7)
	v_mfma_f32_16x16x32_bf16 v[72:75], v[100:103], v[8:11], v[72:75]
	v_mfma_f32_16x16x32_bf16 v[76:79], v[100:103], v[40:43], v[76:79]
	ds_read_b128 v[100:103], v164 offset:8192
	s_waitcnt lgkmcnt(7)
	v_mfma_f32_16x16x32_bf16 v[80:83], v[104:107], v[8:11], v[80:83]
	v_mfma_f32_16x16x32_bf16 v[84:87], v[104:107], v[40:43], v[84:87]
	ds_read_b128 v[104:107], v164 offset:16384
	s_waitcnt lgkmcnt(7)
	v_mfma_f32_16x16x32_bf16 v[88:91], v[108:111], v[8:11], v[88:91]
	v_mfma_f32_16x16x32_bf16 v[92:95], v[108:111], v[40:43], v[92:95]
	ds_read_b128 v[108:111], v164 offset:24576
	s_waitcnt lgkmcnt(7)
	v_mfma_f32_16x16x32_bf16 v[64:67], v[112:115], v[12:15], v[64:67]
	v_mfma_f32_16x16x32_bf16 v[68:71], v[112:115], v[44:47], v[68:71]
	v_xor_b32_e32 v164, 0x140, v163
	ds_read_b128 v[112:115], v164
	s_waitcnt lgkmcnt(7)
	v_mfma_f32_16x16x32_bf16 v[72:75], v[116:119], v[12:15], v[72:75]
	v_mfma_f32_16x16x32_bf16 v[76:79], v[116:119], v[44:47], v[76:79]
	ds_read_b128 v[116:119], v164 offset:8192
	s_waitcnt lgkmcnt(7)
	v_mfma_f32_16x16x32_bf16 v[80:83], v[120:123], v[12:15], v[80:83]
	v_mfma_f32_16x16x32_bf16 v[84:87], v[120:123], v[44:47], v[84:87]
	ds_read_b128 v[120:123], v164 offset:16384
	s_waitcnt lgkmcnt(7)
	v_mfma_f32_16x16x32_bf16 v[88:91], v[124:127], v[12:15], v[88:91]
	v_mfma_f32_16x16x32_bf16 v[92:95], v[124:127], v[44:47], v[92:95]
	ds_read_b128 v[124:127], v164 offset:24576
	s_waitcnt lgkmcnt(7)
	v_mfma_f32_16x16x32_bf16 v[64:67], v[96:99], v[16:19], v[64:67]
	v_mfma_f32_16x16x32_bf16 v[68:71], v[96:99], v[48:51], v[68:71]
	v_xor_b32_e32 v164, 0x180, v163
	ds_read_b128 v[96:99], v164
	s_waitcnt lgkmcnt(7)
	v_mfma_f32_16x16x32_bf16 v[72:75], v[100:103], v[16:19], v[72:75]
	v_mfma_f32_16x16x32_bf16 v[76:79], v[100:103], v[48:51], v[76:79]
	ds_read_b128 v[100:103], v164 offset:8192
	s_waitcnt lgkmcnt(7)
	v_mfma_f32_16x16x32_bf16 v[80:83], v[104:107], v[16:19], v[80:83]
	v_mfma_f32_16x16x32_bf16 v[84:87], v[104:107], v[48:51], v[84:87]
	ds_read_b128 v[104:107], v164 offset:16384
	s_waitcnt lgkmcnt(7)
	v_mfma_f32_16x16x32_bf16 v[88:91], v[108:111], v[16:19], v[88:91]
	v_mfma_f32_16x16x32_bf16 v[92:95], v[108:111], v[48:51], v[92:95]
	ds_read_b128 v[108:111], v164 offset:24576
	s_waitcnt lgkmcnt(7)
	v_mfma_f32_16x16x32_bf16 v[64:67], v[112:115], v[20:23], v[64:67]
	v_mfma_f32_16x16x32_bf16 v[68:71], v[112:115], v[52:55], v[68:71]
	v_xor_b32_e32 v164, 0x1c0, v163
	ds_read_b128 v[112:115], v164
	s_waitcnt lgkmcnt(7)
	v_mfma_f32_16x16x32_bf16 v[72:75], v[116:119], v[20:23], v[72:75]
	v_mfma_f32_16x16x32_bf16 v[76:79], v[116:119], v[52:55], v[76:79]
	ds_read_b128 v[116:119], v164 offset:8192
	s_waitcnt lgkmcnt(7)
	v_mfma_f32_16x16x32_bf16 v[80:83], v[120:123], v[20:23], v[80:83]
	v_mfma_f32_16x16x32_bf16 v[84:87], v[120:123], v[52:55], v[84:87]
	ds_read_b128 v[120:123], v164 offset:16384
	s_waitcnt lgkmcnt(7)
	v_mfma_f32_16x16x32_bf16 v[88:91], v[124:127], v[20:23], v[88:91]
	v_mfma_f32_16x16x32_bf16 v[92:95], v[124:127], v[52:55], v[92:95]
	ds_read_b128 v[124:127], v164 offset:24576
	s_waitcnt lgkmcnt(7)
	v_mfma_f32_16x16x32_bf16 v[64:67], v[96:99], v[24:27], v[64:67]
	v_mfma_f32_16x16x32_bf16 v[68:71], v[96:99], v[56:59], v[68:71]
	s_waitcnt lgkmcnt(6)
	v_mfma_f32_16x16x32_bf16 v[72:75], v[100:103], v[24:27], v[72:75]
	v_mfma_f32_16x16x32_bf16 v[76:79], v[100:103], v[56:59], v[76:79]
	s_waitcnt lgkmcnt(5)
	v_mfma_f32_16x16x32_bf16 v[80:83], v[104:107], v[24:27], v[80:83]
	v_mfma_f32_16x16x32_bf16 v[84:87], v[104:107], v[56:59], v[84:87]
	s_waitcnt lgkmcnt(4)
	v_mfma_f32_16x16x32_bf16 v[88:91], v[108:111], v[24:27], v[88:91]
	v_mfma_f32_16x16x32_bf16 v[92:95], v[108:111], v[56:59], v[92:95]
	s_waitcnt lgkmcnt(3)
	v_mfma_f32_16x16x32_bf16 v[64:67], v[112:115], v[28:31], v[64:67]
	v_mfma_f32_16x16x32_bf16 v[68:71], v[112:115], v[60:63], v[68:71]
	s_waitcnt lgkmcnt(2)
	v_mfma_f32_16x16x32_bf16 v[72:75], v[116:119], v[28:31], v[72:75]
	v_mfma_f32_16x16x32_bf16 v[76:79], v[116:119], v[60:63], v[76:79]
	s_waitcnt lgkmcnt(1)
	v_mfma_f32_16x16x32_bf16 v[80:83], v[120:123], v[28:31], v[80:83]
	v_mfma_f32_16x16x32_bf16 v[84:87], v[120:123], v[60:63], v[84:87]
	s_waitcnt lgkmcnt(0)
	v_mfma_f32_16x16x32_bf16 v[88:91], v[124:127], v[28:31], v[88:91]
	v_mfma_f32_16x16x32_bf16 v[92:95], v[124:127], v[60:63], v[92:95]

.Lmylru_ne_3:
	ds_read_b64 v[178:179], v208
	ds_read_b64 v[180:181], v208 offset:512
	s_waitcnt lgkmcnt(0)
	v_fma_f32 v182, v176, v178, v179
	v_cndmask_b32_e64 v183, v176, v182, s[38:39]
	v_fma_f32 v176, v182, v180, v181
	v_mov_b32_e32 v184, v183
	v_fma_f32 v185, v183, v198, v201
	v_fma_f32 v186, v183, v199, v177
	v_fma_f32 v187, v183, v200, v203
	v_fma_f32 v184, v184, v227, v231
	v_fma_f32 v185, v185, v228, v232
	v_fma_f32 v186, v186, v229, v233
	v_fma_f32 v187, v187, v230, v234
	v_fma_f32 v144, v184, v96, v144
	v_fma_f32 v148, v185, v100, v148
	v_fma_f32 v152, v186, v104, v152
	v_fma_f32 v156, v187, v108, v156
	v_fma_f32 v145, v184, v97, v145
	v_fma_f32 v149, v185, v101, v149
	v_fma_f32 v153, v186, v105, v153
	v_fma_f32 v157, v187, v109, v157
	v_fma_f32 v146, v184, v98, v146
	v_fma_f32 v150, v185, v102, v150
	v_fma_f32 v154, v186, v106, v154
	v_fma_f32 v158, v187, v110, v158
	v_fma_f32 v147, v184, v99, v147
	v_fma_f32 v151, v185, v103, v151
	v_fma_f32 v155, v186, v107, v155
	v_fma_f32 v159, v187, v111, v159
	v_cvt_pk_bf16_f32 v178, v144, v145
	v_cvt_pk_bf16_f32 v179, v146, v147
	v_cvt_pk_bf16_f32 v180, v148, v149
	v_cvt_pk_bf16_f32 v181, v150, v151
	v_cvt_pk_bf16_f32 v182, v152, v153
	v_cvt_pk_bf16_f32 v183, v154, v155
	v_cvt_pk_bf16_f32 v184, v156, v157
	v_cvt_pk_bf16_f32 v185, v158, v159
	global_store_dword v209, v178, s[44:45]
	global_store_dword v209, v179, s[44:45] offset:256
	global_store_dword v209, v180, s[44:45] offset:512
	global_store_dword v209, v181, s[44:45] offset:768
	global_store_dword v209, v182, s[44:45] offset:1024
	global_store_dword v209, v183, s[44:45] offset:1280
	global_store_dword v209, v184, s[44:45] offset:1536
	global_store_dword v209, v185, s[44:45] offset:1792
	s_add_i32 s13, s13, 1
	s_add_i32 s54, s13, -2
	s_lshl_b32 s55, s54, 14
	s_lshl_b32 s56, s6, 11
	s_add_i32 s55, s55, s56
	s_add_u32 s44, s22, s55
	s_addc_u32 s45, s23, 0
	s_cmp_eq_u32 s14, 0
	s_cbranch_scc0 .Lmylru_nm_4
	v_or_b32_e32 v163, 0x10000, v162
	ds_read_b128 v[96:99], v163
	ds_read_b128 v[100:103], v163 offset:8192
	ds_read_b128 v[104:107], v163 offset:16384
	ds_read_b128 v[108:111], v163 offset:24576
	v_xor_b32_e32 v164, 0x40, v163
	ds_read_b128 v[112:115], v164
	ds_read_b128 v[116:119], v164 offset:8192
	ds_read_b128 v[120:123], v164 offset:16384
	ds_read_b128 v[124:127], v164 offset:24576
	s_waitcnt lgkmcnt(7)
	v_mfma_f32_16x16x32_bf16 v[64:67], v[96:99], v[0:3], 0
	v_mfma_f32_16x16x32_bf16 v[68:71], v[96:99], v[32:35], 0
	v_xor_b32_e32 v164, 0x80, v163
	ds_read_b128 v[96:99], v164
	s_waitcnt lgkmcnt(7)
	v_mfma_f32_16x16x32_bf16 v[72:75], v[100:103], v[0:3], 0
	v_mfma_f32_16x16x32_bf16 v[76:79], v[100:103], v[32:35], 0
	ds_read_b128 v[100:103], v164 offset:8192
	s_waitcnt lgkmcnt(7)
	v_mfma_f32_16x16x32_bf16 v[80:83], v[104:107], v[0:3], 0
	v_mfma_f32_16x16x32_bf16 v[84:87], v[104:107], v[32:35], 0
	ds_read_b128 v[104:107], v164 offset:16384
	s_waitcnt lgkmcnt(7)
	v_mfma_f32_16x16x32_bf16 v[88:91], v[108:111], v[0:3], 0
	v_mfma_f32_16x16x32_bf16 v[92:95], v[108:111], v[32:35], 0
	ds_read_b128 v[108:111], v164 offset:24576
	s_waitcnt lgkmcnt(7)
	v_mfma_f32_16x16x32_bf16 v[64:67], v[112:115], v[4:7], v[64:67]
	v_mfma_f32_16x16x32_bf16 v[68:71], v[112:115], v[36:39], v[68:71]
	v_xor_b32_e32 v164, 0xc0, v163
	ds_read_b128 v[112:115], v164
	s_waitcnt lgkmcnt(7)
	v_mfma_f32_16x16x32_bf16 v[72:75], v[116:119], v[4:7], v[72:75]
	v_mfma_f32_16x16x32_bf16 v[76:79], v[116:119], v[36:39], v[76:79]
	ds_read_b128 v[116:119], v164 offset:8192
	s_waitcnt lgkmcnt(7)
	v_mfma_f32_16x16x32_bf16 v[80:83], v[120:123], v[4:7], v[80:83]
	v_mfma_f32_16x16x32_bf16 v[84:87], v[120:123], v[36:39], v[84:87]
	ds_read_b128 v[120:123], v164 offset:16384
	s_waitcnt lgkmcnt(7)
	v_mfma_f32_16x16x32_bf16 v[88:91], v[124:127], v[4:7], v[88:91]
	v_mfma_f32_16x16x32_bf16 v[92:95], v[124:127], v[36:39], v[92:95]
	ds_read_b128 v[124:127], v164 offset:24576
	s_waitcnt lgkmcnt(7)
	v_mfma_f32_16x16x32_bf16 v[64:67], v[96:99], v[8:11], v[64:67]
	v_mfma_f32_16x16x32_bf16 v[68:71], v[96:99], v[40:43], v[68:71]
	v_xor_b32_e32 v164, 0x100, v163
	ds_read_b128 v[96:99], v164
	s_waitcnt lgkmcnt(7)
	v_mfma_f32_16x16x32_bf16 v[72:75], v[100:103], v[8:11], v[72:75]
	v_mfma_f32_16x16x32_bf16 v[76:79], v[100:103], v[40:43], v[76:79]
	ds_read_b128 v[100:103], v164 offset:8192
	s_waitcnt lgkmcnt(7)
	v_mfma_f32_16x16x32_bf16 v[80:83], v[104:107], v[8:11], v[80:83]
	v_mfma_f32_16x16x32_bf16 v[84:87], v[104:107], v[40:43], v[84:87]
	ds_read_b128 v[104:107], v164 offset:16384
	s_waitcnt lgkmcnt(7)
	v_mfma_f32_16x16x32_bf16 v[88:91], v[108:111], v[8:11], v[88:91]
	v_mfma_f32_16x16x32_bf16 v[92:95], v[108:111], v[40:43], v[92:95]
	ds_read_b128 v[108:111], v164 offset:24576
	s_waitcnt lgkmcnt(7)
	v_mfma_f32_16x16x32_bf16 v[64:67], v[112:115], v[12:15], v[64:67]
	v_mfma_f32_16x16x32_bf16 v[68:71], v[112:115], v[44:47], v[68:71]
	v_xor_b32_e32 v164, 0x140, v163
	ds_read_b128 v[112:115], v164
	s_waitcnt lgkmcnt(7)
	v_mfma_f32_16x16x32_bf16 v[72:75], v[116:119], v[12:15], v[72:75]
	v_mfma_f32_16x16x32_bf16 v[76:79], v[116:119], v[44:47], v[76:79]
	ds_read_b128 v[116:119], v164 offset:8192
	s_waitcnt lgkmcnt(7)
	v_mfma_f32_16x16x32_bf16 v[80:83], v[120:123], v[12:15], v[80:83]
	v_mfma_f32_16x16x32_bf16 v[84:87], v[120:123], v[44:47], v[84:87]
	ds_read_b128 v[120:123], v164 offset:16384
	s_waitcnt lgkmcnt(7)
	v_mfma_f32_16x16x32_bf16 v[88:91], v[124:127], v[12:15], v[88:91]
	v_mfma_f32_16x16x32_bf16 v[92:95], v[124:127], v[44:47], v[92:95]
	ds_read_b128 v[124:127], v164 offset:24576
	s_waitcnt lgkmcnt(7)
	v_mfma_f32_16x16x32_bf16 v[64:67], v[96:99], v[16:19], v[64:67]
	v_mfma_f32_16x16x32_bf16 v[68:71], v[96:99], v[48:51], v[68:71]
	v_xor_b32_e32 v164, 0x180, v163
	ds_read_b128 v[96:99], v164
	s_waitcnt lgkmcnt(7)
	v_mfma_f32_16x16x32_bf16 v[72:75], v[100:103], v[16:19], v[72:75]
	v_mfma_f32_16x16x32_bf16 v[76:79], v[100:103], v[48:51], v[76:79]
	ds_read_b128 v[100:103], v164 offset:8192
	s_waitcnt lgkmcnt(7)
	v_mfma_f32_16x16x32_bf16 v[80:83], v[104:107], v[16:19], v[80:83]
	v_mfma_f32_16x16x32_bf16 v[84:87], v[104:107], v[48:51], v[84:87]
	ds_read_b128 v[104:107], v164 offset:16384
	s_waitcnt lgkmcnt(7)
	v_mfma_f32_16x16x32_bf16 v[88:91], v[108:111], v[16:19], v[88:91]
	v_mfma_f32_16x16x32_bf16 v[92:95], v[108:111], v[48:51], v[92:95]
	ds_read_b128 v[108:111], v164 offset:24576
	s_waitcnt lgkmcnt(7)
	v_mfma_f32_16x16x32_bf16 v[64:67], v[112:115], v[20:23], v[64:67]
	v_mfma_f32_16x16x32_bf16 v[68:71], v[112:115], v[52:55], v[68:71]
	v_xor_b32_e32 v164, 0x1c0, v163
	ds_read_b128 v[112:115], v164
	s_waitcnt lgkmcnt(7)
	v_mfma_f32_16x16x32_bf16 v[72:75], v[116:119], v[20:23], v[72:75]
	v_mfma_f32_16x16x32_bf16 v[76:79], v[116:119], v[52:55], v[76:79]
	ds_read_b128 v[116:119], v164 offset:8192
	s_waitcnt lgkmcnt(7)
	v_mfma_f32_16x16x32_bf16 v[80:83], v[120:123], v[20:23], v[80:83]
	v_mfma_f32_16x16x32_bf16 v[84:87], v[120:123], v[52:55], v[84:87]
	ds_read_b128 v[120:123], v164 offset:16384
	s_waitcnt lgkmcnt(7)
	v_mfma_f32_16x16x32_bf16 v[88:91], v[124:127], v[20:23], v[88:91]
	v_mfma_f32_16x16x32_bf16 v[92:95], v[124:127], v[52:55], v[92:95]
	ds_read_b128 v[124:127], v164 offset:24576
	s_waitcnt lgkmcnt(7)
	v_mfma_f32_16x16x32_bf16 v[64:67], v[96:99], v[24:27], v[64:67]
	v_mfma_f32_16x16x32_bf16 v[68:71], v[96:99], v[56:59], v[68:71]
	s_waitcnt lgkmcnt(6)
	v_mfma_f32_16x16x32_bf16 v[72:75], v[100:103], v[24:27], v[72:75]
	v_mfma_f32_16x16x32_bf16 v[76:79], v[100:103], v[56:59], v[76:79]
	s_waitcnt lgkmcnt(5)
	v_mfma_f32_16x16x32_bf16 v[80:83], v[104:107], v[24:27], v[80:83]
	v_mfma_f32_16x16x32_bf16 v[84:87], v[104:107], v[56:59], v[84:87]
	s_waitcnt lgkmcnt(4)
	v_mfma_f32_16x16x32_bf16 v[88:91], v[108:111], v[24:27], v[88:91]
	v_mfma_f32_16x16x32_bf16 v[92:95], v[108:111], v[56:59], v[92:95]
	s_waitcnt lgkmcnt(3)
	v_mfma_f32_16x16x32_bf16 v[64:67], v[112:115], v[28:31], v[64:67]
	v_mfma_f32_16x16x32_bf16 v[68:71], v[112:115], v[60:63], v[68:71]
	s_waitcnt lgkmcnt(2)
	v_mfma_f32_16x16x32_bf16 v[72:75], v[116:119], v[28:31], v[72:75]
	v_mfma_f32_16x16x32_bf16 v[76:79], v[116:119], v[60:63], v[76:79]
	s_waitcnt lgkmcnt(1)
	v_mfma_f32_16x16x32_bf16 v[80:83], v[120:123], v[28:31], v[80:83]
	v_mfma_f32_16x16x32_bf16 v[84:87], v[120:123], v[60:63], v[84:87]
	s_waitcnt lgkmcnt(0)
	v_mfma_f32_16x16x32_bf16 v[88:91], v[124:127], v[28:31], v[88:91]
	v_mfma_f32_16x16x32_bf16 v[92:95], v[124:127], v[60:63], v[92:95]

.Lmylru_ne_4:
	ds_read_b64 v[178:179], v208 offset:1024
	ds_read_b64 v[180:181], v208 offset:1536
	s_waitcnt lgkmcnt(0)
	v_fma_f32 v182, v176, v178, v179
	v_cndmask_b32_e64 v183, v176, v182, s[38:39]
	v_fma_f32 v176, v182, v180, v181
	v_mov_b32_e32 v184, v183
	v_fma_f32 v185, v183, v198, v201
	v_fma_f32 v186, v183, v199, v177
	v_fma_f32 v187, v183, v200, v203
	v_fma_f32 v184, v184, v227, v231
	v_fma_f32 v185, v185, v228, v232
	v_fma_f32 v186, v186, v229, v233
	v_fma_f32 v187, v187, v230, v234
	v_fma_f32 v144, v184, v96, v144
	v_fma_f32 v148, v185, v100, v148
	v_fma_f32 v152, v186, v104, v152
	v_fma_f32 v156, v187, v108, v156
	v_fma_f32 v145, v184, v97, v145
	v_fma_f32 v149, v185, v101, v149
	v_fma_f32 v153, v186, v105, v153
	v_fma_f32 v157, v187, v109, v157
	v_fma_f32 v146, v184, v98, v146
	v_fma_f32 v150, v185, v102, v150
	v_fma_f32 v154, v186, v106, v154
	v_fma_f32 v158, v187, v110, v158
	v_fma_f32 v147, v184, v99, v147
	v_fma_f32 v151, v185, v103, v151
	v_fma_f32 v155, v186, v107, v155
	v_fma_f32 v159, v187, v111, v159
	v_cvt_pk_bf16_f32 v178, v144, v145
	v_cvt_pk_bf16_f32 v179, v146, v147
	v_cvt_pk_bf16_f32 v180, v148, v149
	v_cvt_pk_bf16_f32 v181, v150, v151
	v_cvt_pk_bf16_f32 v182, v152, v153
	v_cvt_pk_bf16_f32 v183, v154, v155
	v_cvt_pk_bf16_f32 v184, v156, v157
	v_cvt_pk_bf16_f32 v185, v158, v159
	global_store_dword v209, v178, s[44:45]
	global_store_dword v209, v179, s[44:45] offset:256
	global_store_dword v209, v180, s[44:45] offset:512
	global_store_dword v209, v181, s[44:45] offset:768
	global_store_dword v209, v182, s[44:45] offset:1024
	global_store_dword v209, v183, s[44:45] offset:1280
	global_store_dword v209, v184, s[44:45] offset:1536
	global_store_dword v209, v185, s[44:45] offset:1792
	s_add_i32 s13, s13, 1
	s_add_i32 s60, s60, -1
	s_cmp_lg_u32 s60, 0
	s_cbranch_scc1 .Lmylru_loop_0
	s_lshl_b32 s50, s10, 10
	s_lshl_b32 s51, s11, 6
	s_add_i32 s50, s50, s51
	s_lshl_b32 s51, s8, 4
	s_add_i32 s50, s50, s51
	s_add_i32 s50, s50, 512
	s_lshl_b32 s50, s50, 9
	s_add_u32 s46, s2, s50
	s_addc_u32 s47, s3, 0
	s_add_u32 s46, s46, 0x1000000
	s_addc_u32 s47, s47, 0
	s_add_u32 s48, s46, 0x20000
	s_addc_u32 s49, s47, 0
	v_lshlrev_b32_e32 v178, 9, v160
	v_lshl_add_u32 v178, v161, 4, v178
	global_load_dwordx4 v[0:3], v178, s[46:47]
	global_load_dwordx4 v[4:7], v178, s[46:47] offset:64
	global_load_dwordx4 v[8:11], v178, s[46:47] offset:128
	global_load_dwordx4 v[12:15], v178, s[46:47] offset:192
	global_load_dwordx4 v[16:19], v178, s[46:47] offset:256
	global_load_dwordx4 v[20:23], v178, s[46:47] offset:320
	global_load_dwordx4 v[24:27], v178, s[46:47] offset:384
	global_load_dwordx4 v[28:31], v178, s[46:47] offset:448
	global_load_dwordx4 v[32:35], v178, s[48:49]
	global_load_dwordx4 v[36:39], v178, s[48:49] offset:64
	global_load_dwordx4 v[40:43], v178, s[48:49] offset:128
	global_load_dwordx4 v[44:47], v178, s[48:49] offset:192
	global_load_dwordx4 v[48:51], v178, s[48:49] offset:256
	global_load_dwordx4 v[52:55], v178, s[48:49] offset:320
	global_load_dwordx4 v[56:59], v178, s[48:49] offset:384
	global_load_dwordx4 v[60:63], v178, s[48:49] offset:448
	s_load_dwordx2 s[46:47], s[0:1], 0xc8
	s_load_dwordx2 s[48:49], s[0:1], 0xd8
	s_load_dwordx2 s[40:41], s[0:1], 0xe0
	s_lshl_b32 s50, s10, 8
	s_lshl_b32 s51, s11, 6
	s_add_i32 s50, s50, s51
	s_lshl_b32 s51, s8, 4
	s_add_i32 s50, s50, s51
	v_add_u32_e32 v179, s50, v160
	v_lshlrev_b32_e32 v179, 2, v179
	s_waitcnt lgkmcnt(0)
	global_load_dword v173, v179, s[46:47]
	global_load_dword v174, v179, s[48:49]
	global_load_dword v175, v179, s[40:41]
	v_cmp_gt_u32_e64 s[34:35], 48, v202
	v_cmp_gt_u32_e64 s[36:37], 32, v202
	v_add_u32_e32 v204, 16, v202
	v_add_u32_e32 v205, 32, v202
	v_mov_b32_e32 v206, v160
	s_cmp_eq_u32 s7, 0
	s_cselect_b64 s[38:39], -1, 0
	v_and_b32_e32 v204, 63, v204
	v_lshlrev_b32_e32 v204, 2, v204
	v_and_b32_e32 v205, 63, v205
	v_lshlrev_b32_e32 v205, 2, v205
	v_and_b32_e32 v206, 63, v206
	v_lshlrev_b32_e32 v206, 2, v206
	v_mov_b32_e32 v176, 0
	s_mov_b32 s53, 0xbfb8aa3b
	s_waitcnt vmcnt(0)
	v_mul_f32_e32 v173, s53, v173
	v_mul_f32_e32 v174, s53, v174
	v_mul_f32_e32 v175, s53, v175
	v_exp_f32_e32 v175, v175
	s_nop 0
	v_add_f32_e32 v180, 1.0, v175
	v_log_f32_e32 v180, v180
	v_mov_b32_e32 v181, 0x3eaaaaab
	v_fma_f32 v181, v175, v181, -0.5
	v_fma_f32 v181, v175, v181, 1.0
	v_mul_f32_e32 v181, v175, v181
	v_mul_f32_e32 v181, 0x3fb8aa3b, v181
	v_cmp_gt_f32_e32 vcc, 0x3cf5c28f, v175
	s_nop 1
	v_cndmask_b32_e32 v175, v180, v181, vcc
	v_mul_f32_e32 v175, 0xc1000000, v175
	s_mov_b32 s13, 0
	s_barrier
	s_cmp_lt_u32 s13, 2
	s_sub_i32 s50, 1, s13
	s_lshl_b32 s50, s50, 7
	s_lshl_b32 s51, s9, 8
	s_add_i32 s51, s51, 0x8000
	s_add_i32 s51, s51, s50
	s_sub_i32 s50, 17, s13
	s_lshl_b32 s50, s50, 7
	s_lshl_b32 s59, s9, 11
	s_add_i32 s59, s59, s50
	s_cmp_lt_u32 s13, 2
	s_cselect_b32 s59, s51, s59
	s_lshl_b32 s52, s59, 11
	s_add_u32 s46, s16, s52
	s_addc_u32 s47, s17, 0
	s_lshl_b32 s52, s6, 13
	s_mov_b32 m0, s52
	s_add_i32 s52, s52, 0x400
	global_load_lds_dwordx4 v211, s[46:47]
	s_mov_b32 m0, s52
	s_add_i32 s52, s52, 0x400
	global_load_lds_dwordx4 v212, s[46:47]
	s_mov_b32 m0, s52
	s_add_i32 s52, s52, 0x400
	global_load_lds_dwordx4 v213, s[46:47]
	s_mov_b32 m0, s52
	s_add_i32 s52, s52, 0x400
	global_load_lds_dwordx4 v214, s[46:47]
	s_mov_b32 m0, s52
	s_add_i32 s52, s52, 0x400
	global_load_lds_dwordx4 v215, s[46:47]
	s_mov_b32 m0, s52
	s_add_i32 s52, s52, 0x400
	global_load_lds_dwordx4 v216, s[46:47]
	s_mov_b32 m0, s52
	s_add_i32 s52, s52, 0x400
	global_load_lds_dwordx4 v217, s[46:47]
	s_mov_b32 m0, s52
	s_nop 0
	global_load_lds_dwordx4 v218, s[46:47]
	s_mov_b32 s58, 1
	s_cmp_lt_u32 s58, 2
	s_sub_i32 s50, 1, s58
	s_lshl_b32 s50, s50, 7
	s_lshl_b32 s51, s9, 8
	s_add_i32 s51, s51, 0x8000
	s_add_i32 s51, s51, s50
	s_sub_i32 s50, 17, s58
	s_lshl_b32 s50, s50, 7
	s_lshl_b32 s59, s9, 11
	s_add_i32 s59, s59, s50
	s_cmp_lt_u32 s58, 2
	s_cselect_b32 s59, s51, s59
	s_lshl_b32 s52, s59, 11
	s_add_u32 s46, s16, s52
	s_addc_u32 s47, s17, 0
	s_lshl_b32 s52, s6, 13
	s_add_i32 s52, s52, 0x10000
	s_mov_b32 m0, s52
	s_add_i32 s52, s52, 0x400
	global_load_lds_dwordx4 v211, s[46:47]
	s_mov_b32 m0, s52
	s_add_i32 s52, s52, 0x400
	global_load_lds_dwordx4 v212, s[46:47]
	s_mov_b32 m0, s52
	s_add_i32 s52, s52, 0x400
	global_load_lds_dwordx4 v213, s[46:47]
	s_mov_b32 m0, s52
	s_add_i32 s52, s52, 0x400
	global_load_lds_dwordx4 v214, s[46:47]
	s_mov_b32 m0, s52
	s_add_i32 s52, s52, 0x400
	global_load_lds_dwordx4 v215, s[46:47]
	s_mov_b32 m0, s52
	s_add_i32 s52, s52, 0x400
	global_load_lds_dwordx4 v216, s[46:47]
	s_mov_b32 m0, s52
	s_add_i32 s52, s52, 0x400
	global_load_lds_dwordx4 v217, s[46:47]
	s_mov_b32 m0, s52
	s_nop 0
	global_load_lds_dwordx4 v218, s[46:47]
	s_waitcnt vmcnt(8)
	s_barrier
	s_cmp_eq_u32 s14, 0
	s_cbranch_scc1 .Lmylru_p0_1
	v_mov_b32_e32 v163, v162
	ds_read_b128 v[112:115], v163
	ds_read_b128 v[116:119], v163 offset:8192
	ds_read_b128 v[120:123], v163 offset:16384
	ds_read_b128 v[124:127], v163 offset:24576
	s_waitcnt lgkmcnt(3)
	v_mfma_f32_16x16x32_bf16 v[64:67], v[112:115], v[0:3], 0
	v_mfma_f32_16x16x32_bf16 v[68:71], v[112:115], v[32:35], 0
	v_xor_b32_e32 v164, 0x40, v163
	ds_read_b128 v[112:115], v164
	s_waitcnt lgkmcnt(3)
	v_mfma_f32_16x16x32_bf16 v[72:75], v[116:119], v[0:3], 0
	v_mfma_f32_16x16x32_bf16 v[76:79], v[116:119], v[32:35], 0
	ds_read_b128 v[116:119], v164 offset:8192
	s_waitcnt lgkmcnt(3)
	v_mfma_f32_16x16x32_bf16 v[80:83], v[120:123], v[0:3], 0
	v_mfma_f32_16x16x32_bf16 v[84:87], v[120:123], v[32:35], 0
	ds_read_b128 v[120:123], v164 offset:16384
	s_waitcnt lgkmcnt(3)
	v_mfma_f32_16x16x32_bf16 v[88:91], v[124:127], v[0:3], 0
	v_mfma_f32_16x16x32_bf16 v[92:95], v[124:127], v[32:35], 0
	ds_read_b128 v[124:127], v164 offset:24576
	s_waitcnt lgkmcnt(3)
	v_mfma_f32_16x16x32_bf16 v[64:67], v[112:115], v[4:7], v[64:67]
	v_mfma_f32_16x16x32_bf16 v[68:71], v[112:115], v[36:39], v[68:71]
	v_xor_b32_e32 v164, 0x80, v163
	ds_read_b128 v[112:115], v164
	s_waitcnt lgkmcnt(3)
	v_mfma_f32_16x16x32_bf16 v[72:75], v[116:119], v[4:7], v[72:75]
	v_mfma_f32_16x16x32_bf16 v[76:79], v[116:119], v[36:39], v[76:79]
	ds_read_b128 v[116:119], v164 offset:8192
	s_waitcnt lgkmcnt(3)
	v_mfma_f32_16x16x32_bf16 v[80:83], v[120:123], v[4:7], v[80:83]
	v_mfma_f32_16x16x32_bf16 v[84:87], v[120:123], v[36:39], v[84:87]
	ds_read_b128 v[120:123], v164 offset:16384
	s_waitcnt lgkmcnt(3)
	v_mfma_f32_16x16x32_bf16 v[88:91], v[124:127], v[4:7], v[88:91]
	v_mfma_f32_16x16x32_bf16 v[92:95], v[124:127], v[36:39], v[92:95]
	ds_read_b128 v[124:127], v164 offset:24576
	s_waitcnt lgkmcnt(3)
	v_mfma_f32_16x16x32_bf16 v[64:67], v[112:115], v[8:11], v[64:67]
	v_mfma_f32_16x16x32_bf16 v[68:71], v[112:115], v[40:43], v[68:71]
	v_xor_b32_e32 v164, 0xc0, v163
	ds_read_b128 v[112:115], v164
	s_waitcnt lgkmcnt(3)
	v_mfma_f32_16x16x32_bf16 v[72:75], v[116:119], v[8:11], v[72:75]
	v_mfma_f32_16x16x32_bf16 v[76:79], v[116:119], v[40:43], v[76:79]
	ds_read_b128 v[116:119], v164 offset:8192
	s_waitcnt lgkmcnt(3)
	v_mfma_f32_16x16x32_bf16 v[80:83], v[120:123], v[8:11], v[80:83]
	v_mfma_f32_16x16x32_bf16 v[84:87], v[120:123], v[40:43], v[84:87]
	ds_read_b128 v[120:123], v164 offset:16384
	s_waitcnt lgkmcnt(3)
	v_mfma_f32_16x16x32_bf16 v[88:91], v[124:127], v[8:11], v[88:91]
	v_mfma_f32_16x16x32_bf16 v[92:95], v[124:127], v[40:43], v[92:95]
	ds_read_b128 v[124:127], v164 offset:24576
	s_waitcnt lgkmcnt(3)
	v_mfma_f32_16x16x32_bf16 v[64:67], v[112:115], v[12:15], v[64:67]
	v_mfma_f32_16x16x32_bf16 v[68:71], v[112:115], v[44:47], v[68:71]
	v_xor_b32_e32 v164, 0x100, v163
	ds_read_b128 v[112:115], v164
	s_waitcnt lgkmcnt(3)
	v_mfma_f32_16x16x32_bf16 v[72:75], v[116:119], v[12:15], v[72:75]
	v_mfma_f32_16x16x32_bf16 v[76:79], v[116:119], v[44:47], v[76:79]
	ds_read_b128 v[116:119], v164 offset:8192
	s_waitcnt lgkmcnt(3)
	v_mfma_f32_16x16x32_bf16 v[80:83], v[120:123], v[12:15], v[80:83]
	v_mfma_f32_16x16x32_bf16 v[84:87], v[120:123], v[44:47], v[84:87]
	ds_read_b128 v[120:123], v164 offset:16384
	s_waitcnt lgkmcnt(3)
	v_mfma_f32_16x16x32_bf16 v[88:91], v[124:127], v[12:15], v[88:91]
	v_mfma_f32_16x16x32_bf16 v[92:95], v[124:127], v[44:47], v[92:95]
	ds_read_b128 v[124:127], v164 offset:24576
	s_waitcnt lgkmcnt(3)
	v_mfma_f32_16x16x32_bf16 v[64:67], v[112:115], v[16:19], v[64:67]
	v_mfma_f32_16x16x32_bf16 v[68:71], v[112:115], v[48:51], v[68:71]
	v_xor_b32_e32 v164, 0x140, v163
	ds_read_b128 v[112:115], v164
	s_waitcnt lgkmcnt(3)
	v_mfma_f32_16x16x32_bf16 v[72:75], v[116:119], v[16:19], v[72:75]
	v_mfma_f32_16x16x32_bf16 v[76:79], v[116:119], v[48:51], v[76:79]
	ds_read_b128 v[116:119], v164 offset:8192
	s_waitcnt lgkmcnt(3)
	v_mfma_f32_16x16x32_bf16 v[80:83], v[120:123], v[16:19], v[80:83]
	v_mfma_f32_16x16x32_bf16 v[84:87], v[120:123], v[48:51], v[84:87]
	ds_read_b128 v[120:123], v164 offset:16384
	s_waitcnt lgkmcnt(3)
	v_mfma_f32_16x16x32_bf16 v[88:91], v[124:127], v[16:19], v[88:91]
	v_mfma_f32_16x16x32_bf16 v[92:95], v[124:127], v[48:51], v[92:95]
	ds_read_b128 v[124:127], v164 offset:24576
	s_waitcnt lgkmcnt(3)
	v_mfma_f32_16x16x32_bf16 v[64:67], v[112:115], v[20:23], v[64:67]
	v_mfma_f32_16x16x32_bf16 v[68:71], v[112:115], v[52:55], v[68:71]
	v_xor_b32_e32 v164, 0x180, v163
	ds_read_b128 v[112:115], v164
	s_waitcnt lgkmcnt(3)
	v_mfma_f32_16x16x32_bf16 v[72:75], v[116:119], v[20:23], v[72:75]
	v_mfma_f32_16x16x32_bf16 v[76:79], v[116:119], v[52:55], v[76:79]
	ds_read_b128 v[116:119], v164 offset:8192
	s_waitcnt lgkmcnt(3)
	v_mfma_f32_16x16x32_bf16 v[80:83], v[120:123], v[20:23], v[80:83]
	v_mfma_f32_16x16x32_bf16 v[84:87], v[120:123], v[52:55], v[84:87]
	ds_read_b128 v[120:123], v164 offset:16384
	s_waitcnt lgkmcnt(3)
	v_mfma_f32_16x16x32_bf16 v[88:91], v[124:127], v[20:23], v[88:91]
	v_mfma_f32_16x16x32_bf16 v[92:95], v[124:127], v[52:55], v[92:95]
	ds_read_b128 v[124:127], v164 offset:24576
	s_waitcnt lgkmcnt(3)
	v_mfma_f32_16x16x32_bf16 v[64:67], v[112:115], v[24:27], v[64:67]
	v_mfma_f32_16x16x32_bf16 v[68:71], v[112:115], v[56:59], v[68:71]
	v_xor_b32_e32 v164, 0x1c0, v163
	ds_read_b128 v[112:115], v164
	s_waitcnt lgkmcnt(3)
	v_mfma_f32_16x16x32_bf16 v[72:75], v[116:119], v[24:27], v[72:75]
	v_mfma_f32_16x16x32_bf16 v[76:79], v[116:119], v[56:59], v[76:79]
	ds_read_b128 v[116:119], v164 offset:8192
	s_waitcnt lgkmcnt(3)
	v_mfma_f32_16x16x32_bf16 v[80:83], v[120:123], v[24:27], v[80:83]
	v_mfma_f32_16x16x32_bf16 v[84:87], v[120:123], v[56:59], v[84:87]
	ds_read_b128 v[120:123], v164 offset:16384
	s_waitcnt lgkmcnt(3)
	v_mfma_f32_16x16x32_bf16 v[88:91], v[124:127], v[24:27], v[88:91]
	v_mfma_f32_16x16x32_bf16 v[92:95], v[124:127], v[56:59], v[92:95]
	ds_read_b128 v[124:127], v164 offset:24576
	s_waitcnt lgkmcnt(3)
	v_mfma_f32_16x16x32_bf16 v[64:67], v[112:115], v[28:31], v[64:67]
	v_mfma_f32_16x16x32_bf16 v[68:71], v[112:115], v[60:63], v[68:71]
	s_waitcnt lgkmcnt(2)
	v_mfma_f32_16x16x32_bf16 v[72:75], v[116:119], v[28:31], v[72:75]
	v_mfma_f32_16x16x32_bf16 v[76:79], v[116:119], v[60:63], v[76:79]
	s_waitcnt lgkmcnt(1)
	v_mfma_f32_16x16x32_bf16 v[80:83], v[120:123], v[28:31], v[80:83]
	v_mfma_f32_16x16x32_bf16 v[84:87], v[120:123], v[60:63], v[84:87]
	s_waitcnt lgkmcnt(0)
	v_mfma_f32_16x16x32_bf16 v[88:91], v[124:127], v[28:31], v[88:91]
	v_mfma_f32_16x16x32_bf16 v[92:95], v[124:127], v[60:63], v[92:95]

.Lmylru_ne_5:
	ds_read_b64 v[178:179], v208 offset:512
	ds_read_b64 v[180:181], v208
	s_waitcnt lgkmcnt(0)
	v_fma_f32 v182, v176, v178, v179
	v_cndmask_b32_e64 v183, v176, v182, s[38:39]
	v_fma_f32 v176, v182, v180, v181
	s_add_i32 s13, s13, 1
	s_cmp_eq_u32 s14, 0
	s_cbranch_scc0 .Lmylru_nm_6
	v_or_b32_e32 v163, 0x10000, v162
	ds_read_b128 v[96:99], v163
	ds_read_b128 v[100:103], v163 offset:8192
	ds_read_b128 v[104:107], v163 offset:16384
	ds_read_b128 v[108:111], v163 offset:24576
	v_xor_b32_e32 v164, 0x40, v163
	ds_read_b128 v[112:115], v164
	ds_read_b128 v[116:119], v164 offset:8192
	ds_read_b128 v[120:123], v164 offset:16384
	ds_read_b128 v[124:127], v164 offset:24576
	s_waitcnt lgkmcnt(7)
	v_mfma_f32_16x16x32_bf16 v[64:67], v[96:99], v[0:3], 0
	v_mfma_f32_16x16x32_bf16 v[68:71], v[96:99], v[32:35], 0
	v_xor_b32_e32 v164, 0x80, v163
	ds_read_b128 v[96:99], v164
	s_waitcnt lgkmcnt(7)
	v_mfma_f32_16x16x32_bf16 v[72:75], v[100:103], v[0:3], 0
	v_mfma_f32_16x16x32_bf16 v[76:79], v[100:103], v[32:35], 0
	ds_read_b128 v[100:103], v164 offset:8192
	s_waitcnt lgkmcnt(7)
	v_mfma_f32_16x16x32_bf16 v[80:83], v[104:107], v[0:3], 0
	v_mfma_f32_16x16x32_bf16 v[84:87], v[104:107], v[32:35], 0
	ds_read_b128 v[104:107], v164 offset:16384
	s_waitcnt lgkmcnt(7)
	v_mfma_f32_16x16x32_bf16 v[88:91], v[108:111], v[0:3], 0
	v_mfma_f32_16x16x32_bf16 v[92:95], v[108:111], v[32:35], 0
	ds_read_b128 v[108:111], v164 offset:24576
	s_waitcnt lgkmcnt(7)
	v_mfma_f32_16x16x32_bf16 v[64:67], v[112:115], v[4:7], v[64:67]
	v_mfma_f32_16x16x32_bf16 v[68:71], v[112:115], v[36:39], v[68:71]
	v_xor_b32_e32 v164, 0xc0, v163
	ds_read_b128 v[112:115], v164
	s_waitcnt lgkmcnt(7)
	v_mfma_f32_16x16x32_bf16 v[72:75], v[116:119], v[4:7], v[72:75]
	v_mfma_f32_16x16x32_bf16 v[76:79], v[116:119], v[36:39], v[76:79]
	ds_read_b128 v[116:119], v164 offset:8192
	s_waitcnt lgkmcnt(7)
	v_mfma_f32_16x16x32_bf16 v[80:83], v[120:123], v[4:7], v[80:83]
	v_mfma_f32_16x16x32_bf16 v[84:87], v[120:123], v[36:39], v[84:87]
	ds_read_b128 v[120:123], v164 offset:16384
	s_waitcnt lgkmcnt(7)
	v_mfma_f32_16x16x32_bf16 v[88:91], v[124:127], v[4:7], v[88:91]
	v_mfma_f32_16x16x32_bf16 v[92:95], v[124:127], v[36:39], v[92:95]
	ds_read_b128 v[124:127], v164 offset:24576
	s_waitcnt lgkmcnt(7)
	v_mfma_f32_16x16x32_bf16 v[64:67], v[96:99], v[8:11], v[64:67]
	v_mfma_f32_16x16x32_bf16 v[68:71], v[96:99], v[40:43], v[68:71]
	v_xor_b32_e32 v164, 0x100, v163
	ds_read_b128 v[96:99], v164
	s_waitcnt lgkmcnt(7)
	v_mfma_f32_16x16x32_bf16 v[72:75], v[100:103], v[8:11], v[72:75]
	v_mfma_f32_16x16x32_bf16 v[76:79], v[100:103], v[40:43], v[76:79]
	ds_read_b128 v[100:103], v164 offset:8192
	s_waitcnt lgkmcnt(7)
	v_mfma_f32_16x16x32_bf16 v[80:83], v[104:107], v[8:11], v[80:83]
	v_mfma_f32_16x16x32_bf16 v[84:87], v[104:107], v[40:43], v[84:87]
	ds_read_b128 v[104:107], v164 offset:16384
	s_waitcnt lgkmcnt(7)
	v_mfma_f32_16x16x32_bf16 v[88:91], v[108:111], v[8:11], v[88:91]
	v_mfma_f32_16x16x32_bf16 v[92:95], v[108:111], v[40:43], v[92:95]
	ds_read_b128 v[108:111], v164 offset:24576
	s_waitcnt lgkmcnt(7)
	v_mfma_f32_16x16x32_bf16 v[64:67], v[112:115], v[12:15], v[64:67]
	v_mfma_f32_16x16x32_bf16 v[68:71], v[112:115], v[44:47], v[68:71]
	v_xor_b32_e32 v164, 0x140, v163
	ds_read_b128 v[112:115], v164
	s_waitcnt lgkmcnt(7)
	v_mfma_f32_16x16x32_bf16 v[72:75], v[116:119], v[12:15], v[72:75]
	v_mfma_f32_16x16x32_bf16 v[76:79], v[116:119], v[44:47], v[76:79]
	ds_read_b128 v[116:119], v164 offset:8192
	s_waitcnt lgkmcnt(7)
	v_mfma_f32_16x16x32_bf16 v[80:83], v[120:123], v[12:15], v[80:83]
	v_mfma_f32_16x16x32_bf16 v[84:87], v[120:123], v[44:47], v[84:87]
	ds_read_b128 v[120:123], v164 offset:16384
	s_waitcnt lgkmcnt(7)
	v_mfma_f32_16x16x32_bf16 v[88:91], v[124:127], v[12:15], v[88:91]
	v_mfma_f32_16x16x32_bf16 v[92:95], v[124:127], v[44:47], v[92:95]
	ds_read_b128 v[124:127], v164 offset:24576
	s_waitcnt lgkmcnt(7)
	v_mfma_f32_16x16x32_bf16 v[64:67], v[96:99], v[16:19], v[64:67]
	v_mfma_f32_16x16x32_bf16 v[68:71], v[96:99], v[48:51], v[68:71]
	v_xor_b32_e32 v164, 0x180, v163
	ds_read_b128 v[96:99], v164
	s_waitcnt lgkmcnt(7)
	v_mfma_f32_16x16x32_bf16 v[72:75], v[100:103], v[16:19], v[72:75]
	v_mfma_f32_16x16x32_bf16 v[76:79], v[100:103], v[48:51], v[76:79]
	ds_read_b128 v[100:103], v164 offset:8192
	s_waitcnt lgkmcnt(7)
	v_mfma_f32_16x16x32_bf16 v[80:83], v[104:107], v[16:19], v[80:83]
	v_mfma_f32_16x16x32_bf16 v[84:87], v[104:107], v[48:51], v[84:87]
	ds_read_b128 v[104:107], v164 offset:16384
	s_waitcnt lgkmcnt(7)
	v_mfma_f32_16x16x32_bf16 v[88:91], v[108:111], v[16:19], v[88:91]
	v_mfma_f32_16x16x32_bf16 v[92:95], v[108:111], v[48:51], v[92:95]
	ds_read_b128 v[108:111], v164 offset:24576
	s_waitcnt lgkmcnt(7)
	v_mfma_f32_16x16x32_bf16 v[64:67], v[112:115], v[20:23], v[64:67]
	v_mfma_f32_16x16x32_bf16 v[68:71], v[112:115], v[52:55], v[68:71]
	v_xor_b32_e32 v164, 0x1c0, v163
	ds_read_b128 v[112:115], v164
	s_waitcnt lgkmcnt(7)
	v_mfma_f32_16x16x32_bf16 v[72:75], v[116:119], v[20:23], v[72:75]
	v_mfma_f32_16x16x32_bf16 v[76:79], v[116:119], v[52:55], v[76:79]
	ds_read_b128 v[116:119], v164 offset:8192
	s_waitcnt lgkmcnt(7)
	v_mfma_f32_16x16x32_bf16 v[80:83], v[120:123], v[20:23], v[80:83]
	v_mfma_f32_16x16x32_bf16 v[84:87], v[120:123], v[52:55], v[84:87]
	ds_read_b128 v[120:123], v164 offset:16384
	s_waitcnt lgkmcnt(7)
	v_mfma_f32_16x16x32_bf16 v[88:91], v[124:127], v[20:23], v[88:91]
	v_mfma_f32_16x16x32_bf16 v[92:95], v[124:127], v[52:55], v[92:95]
	ds_read_b128 v[124:127], v164 offset:24576
	s_waitcnt lgkmcnt(7)
	v_mfma_f32_16x16x32_bf16 v[64:67], v[96:99], v[24:27], v[64:67]
	v_mfma_f32_16x16x32_bf16 v[68:71], v[96:99], v[56:59], v[68:71]
	s_waitcnt lgkmcnt(6)
	v_mfma_f32_16x16x32_bf16 v[72:75], v[100:103], v[24:27], v[72:75]
	v_mfma_f32_16x16x32_bf16 v[76:79], v[100:103], v[56:59], v[76:79]
	s_waitcnt lgkmcnt(5)
	v_mfma_f32_16x16x32_bf16 v[80:83], v[104:107], v[24:27], v[80:83]
	v_mfma_f32_16x16x32_bf16 v[84:87], v[104:107], v[56:59], v[84:87]
	s_waitcnt lgkmcnt(4)
	v_mfma_f32_16x16x32_bf16 v[88:91], v[108:111], v[24:27], v[88:91]
	v_mfma_f32_16x16x32_bf16 v[92:95], v[108:111], v[56:59], v[92:95]
	s_waitcnt lgkmcnt(3)
	v_mfma_f32_16x16x32_bf16 v[64:67], v[112:115], v[28:31], v[64:67]
	v_mfma_f32_16x16x32_bf16 v[68:71], v[112:115], v[60:63], v[68:71]
	s_waitcnt lgkmcnt(2)
	v_mfma_f32_16x16x32_bf16 v[72:75], v[116:119], v[28:31], v[72:75]
	v_mfma_f32_16x16x32_bf16 v[76:79], v[116:119], v[60:63], v[76:79]
	s_waitcnt lgkmcnt(1)
	v_mfma_f32_16x16x32_bf16 v[80:83], v[120:123], v[28:31], v[80:83]
	v_mfma_f32_16x16x32_bf16 v[84:87], v[120:123], v[60:63], v[84:87]
	s_waitcnt lgkmcnt(0)
	v_mfma_f32_16x16x32_bf16 v[88:91], v[124:127], v[28:31], v[88:91]
	v_mfma_f32_16x16x32_bf16 v[92:95], v[124:127], v[60:63], v[92:95]

.Lmylru_loop_1:
	s_sub_i32 s54, 17, s13
	s_lshl_b32 s55, s54, 14
	s_lshl_b32 s56, s6, 11
	s_add_i32 s55, s55, s56
	s_add_u32 s44, s22, s55
	s_addc_u32 s45, s23, 0
	s_cmp_lt_u32 s13, 2
	s_sub_i32 s50, 1, s13
	s_lshl_b32 s50, s50, 7
	s_lshl_b32 s51, s9, 8
	s_add_i32 s51, s51, 0x8000
	s_add_i32 s51, s51, s50
	s_sub_i32 s50, 17, s13
	s_lshl_b32 s50, s50, 7
	s_lshl_b32 s57, s9, 11
	s_add_i32 s57, s57, s50
	s_cmp_lt_u32 s13, 2
	s_cselect_b32 s57, s51, s57
	s_lshl_b32 s57, s57, 11
	s_add_u32 s40, s18, s57
	s_addc_u32 s41, s19, 0
	s_add_u32 s42, s20, s57
	s_addc_u32 s43, s21, 0
	global_load_dword v247, v209, s[44:45]
	global_load_dword v248, v209, s[44:45] offset:256
	global_load_dword v249, v209, s[44:45] offset:512
	global_load_dword v250, v209, s[44:45] offset:768
	global_load_dword v251, v209, s[44:45] offset:1024
	global_load_dword v252, v209, s[44:45] offset:1280
	global_load_dword v253, v209, s[44:45] offset:1536
	global_load_dword v254, v209, s[44:45] offset:1792
	v_add_u32_e32 v182, 0x0, v210
	v_add_u32_e32 v183, 0x1000, v182
	global_load_ushort v128, v182, s[40:41]
	global_load_ushort v129, v182, s[40:41] offset:2048
	global_load_ushort v130, v183, s[40:41]
	global_load_ushort v131, v183, s[40:41] offset:2048
	v_add_u32_e32 v182, 0x8000, v210
	v_add_u32_e32 v183, 0x1000, v182
	global_load_ushort v132, v182, s[40:41]
	global_load_ushort v133, v182, s[40:41] offset:2048
	global_load_ushort v134, v183, s[40:41]
	global_load_ushort v135, v183, s[40:41] offset:2048
	v_add_u32_e32 v182, 0x10000, v210
	v_add_u32_e32 v183, 0x1000, v182
	global_load_ushort v136, v182, s[40:41]
	global_load_ushort v137, v182, s[40:41] offset:2048
	global_load_ushort v138, v183, s[40:41]
	global_load_ushort v139, v183, s[40:41] offset:2048
	v_add_u32_e32 v182, 0x18000, v210
	v_add_u32_e32 v183, 0x1000, v182
	global_load_ushort v140, v182, s[40:41]
	global_load_ushort v141, v182, s[40:41] offset:2048
	global_load_ushort v142, v183, s[40:41]
	global_load_ushort v143, v183, s[40:41] offset:2048
	s_cmp_eq_u32 s14, 0
	s_cbranch_scc0 .Lmylru_nm_7
	v_mov_b32_e32 v163, v162
	ds_read_b128 v[96:99], v163
	ds_read_b128 v[100:103], v163 offset:8192
	ds_read_b128 v[104:107], v163 offset:16384
	ds_read_b128 v[108:111], v163 offset:24576
	v_xor_b32_e32 v164, 0x40, v163
	ds_read_b128 v[112:115], v164
	ds_read_b128 v[116:119], v164 offset:8192
	ds_read_b128 v[120:123], v164 offset:16384
	ds_read_b128 v[124:127], v164 offset:24576
	s_waitcnt lgkmcnt(7)
	v_mfma_f32_16x16x32_bf16 v[64:67], v[96:99], v[0:3], 0
	v_mfma_f32_16x16x32_bf16 v[68:71], v[96:99], v[32:35], 0
	v_xor_b32_e32 v164, 0x80, v163
	ds_read_b128 v[96:99], v164
	s_waitcnt lgkmcnt(7)
	v_mfma_f32_16x16x32_bf16 v[72:75], v[100:103], v[0:3], 0
	v_mfma_f32_16x16x32_bf16 v[76:79], v[100:103], v[32:35], 0
	ds_read_b128 v[100:103], v164 offset:8192
	s_waitcnt lgkmcnt(7)
	v_mfma_f32_16x16x32_bf16 v[80:83], v[104:107], v[0:3], 0
	v_mfma_f32_16x16x32_bf16 v[84:87], v[104:107], v[32:35], 0
	ds_read_b128 v[104:107], v164 offset:16384
	s_waitcnt lgkmcnt(7)
	v_mfma_f32_16x16x32_bf16 v[88:91], v[108:111], v[0:3], 0
	v_mfma_f32_16x16x32_bf16 v[92:95], v[108:111], v[32:35], 0
	ds_read_b128 v[108:111], v164 offset:24576
	s_waitcnt lgkmcnt(7)
	v_mfma_f32_16x16x32_bf16 v[64:67], v[112:115], v[4:7], v[64:67]
	v_mfma_f32_16x16x32_bf16 v[68:71], v[112:115], v[36:39], v[68:71]
	v_xor_b32_e32 v164, 0xc0, v163
	ds_read_b128 v[112:115], v164
	s_waitcnt lgkmcnt(7)
	v_mfma_f32_16x16x32_bf16 v[72:75], v[116:119], v[4:7], v[72:75]
	v_mfma_f32_16x16x32_bf16 v[76:79], v[116:119], v[36:39], v[76:79]
	ds_read_b128 v[116:119], v164 offset:8192
	s_waitcnt lgkmcnt(7)
	v_mfma_f32_16x16x32_bf16 v[80:83], v[120:123], v[4:7], v[80:83]
	v_mfma_f32_16x16x32_bf16 v[84:87], v[120:123], v[36:39], v[84:87]
	ds_read_b128 v[120:123], v164 offset:16384
	s_waitcnt lgkmcnt(7)
	v_mfma_f32_16x16x32_bf16 v[88:91], v[124:127], v[4:7], v[88:91]
	v_mfma_f32_16x16x32_bf16 v[92:95], v[124:127], v[36:39], v[92:95]
	ds_read_b128 v[124:127], v164 offset:24576
	s_waitcnt lgkmcnt(7)
	v_mfma_f32_16x16x32_bf16 v[64:67], v[96:99], v[8:11], v[64:67]
	v_mfma_f32_16x16x32_bf16 v[68:71], v[96:99], v[40:43], v[68:71]
	v_xor_b32_e32 v164, 0x100, v163
	ds_read_b128 v[96:99], v164
	s_waitcnt lgkmcnt(7)
	v_mfma_f32_16x16x32_bf16 v[72:75], v[100:103], v[8:11], v[72:75]
	v_mfma_f32_16x16x32_bf16 v[76:79], v[100:103], v[40:43], v[76:79]
	ds_read_b128 v[100:103], v164 offset:8192
	s_waitcnt lgkmcnt(7)
	v_mfma_f32_16x16x32_bf16 v[80:83], v[104:107], v[8:11], v[80:83]
	v_mfma_f32_16x16x32_bf16 v[84:87], v[104:107], v[40:43], v[84:87]
	ds_read_b128 v[104:107], v164 offset:16384
	s_waitcnt lgkmcnt(7)
	v_mfma_f32_16x16x32_bf16 v[88:91], v[108:111], v[8:11], v[88:91]
	v_mfma_f32_16x16x32_bf16 v[92:95], v[108:111], v[40:43], v[92:95]
	ds_read_b128 v[108:111], v164 offset:24576
	s_waitcnt lgkmcnt(7)
	v_mfma_f32_16x16x32_bf16 v[64:67], v[112:115], v[12:15], v[64:67]
	v_mfma_f32_16x16x32_bf16 v[68:71], v[112:115], v[44:47], v[68:71]
	v_xor_b32_e32 v164, 0x140, v163
	ds_read_b128 v[112:115], v164
	s_waitcnt lgkmcnt(7)
	v_mfma_f32_16x16x32_bf16 v[72:75], v[116:119], v[12:15], v[72:75]
	v_mfma_f32_16x16x32_bf16 v[76:79], v[116:119], v[44:47], v[76:79]
	ds_read_b128 v[116:119], v164 offset:8192
	s_waitcnt lgkmcnt(7)
	v_mfma_f32_16x16x32_bf16 v[80:83], v[120:123], v[12:15], v[80:83]
	v_mfma_f32_16x16x32_bf16 v[84:87], v[120:123], v[44:47], v[84:87]
	ds_read_b128 v[120:123], v164 offset:16384
	s_waitcnt lgkmcnt(7)
	v_mfma_f32_16x16x32_bf16 v[88:91], v[124:127], v[12:15], v[88:91]
	v_mfma_f32_16x16x32_bf16 v[92:95], v[124:127], v[44:47], v[92:95]
	ds_read_b128 v[124:127], v164 offset:24576
	s_waitcnt lgkmcnt(7)
	v_mfma_f32_16x16x32_bf16 v[64:67], v[96:99], v[16:19], v[64:67]
	v_mfma_f32_16x16x32_bf16 v[68:71], v[96:99], v[48:51], v[68:71]
	v_xor_b32_e32 v164, 0x180, v163
	ds_read_b128 v[96:99], v164
	s_waitcnt lgkmcnt(7)
	v_mfma_f32_16x16x32_bf16 v[72:75], v[100:103], v[16:19], v[72:75]
	v_mfma_f32_16x16x32_bf16 v[76:79], v[100:103], v[48:51], v[76:79]
	ds_read_b128 v[100:103], v164 offset:8192
	s_waitcnt lgkmcnt(7)
	v_mfma_f32_16x16x32_bf16 v[80:83], v[104:107], v[16:19], v[80:83]
	v_mfma_f32_16x16x32_bf16 v[84:87], v[104:107], v[48:51], v[84:87]
	ds_read_b128 v[104:107], v164 offset:16384
	s_waitcnt lgkmcnt(7)
	v_mfma_f32_16x16x32_bf16 v[88:91], v[108:111], v[16:19], v[88:91]
	v_mfma_f32_16x16x32_bf16 v[92:95], v[108:111], v[48:51], v[92:95]
	ds_read_b128 v[108:111], v164 offset:24576
	s_waitcnt lgkmcnt(7)
	v_mfma_f32_16x16x32_bf16 v[64:67], v[112:115], v[20:23], v[64:67]
	v_mfma_f32_16x16x32_bf16 v[68:71], v[112:115], v[52:55], v[68:71]
	v_xor_b32_e32 v164, 0x1c0, v163
	ds_read_b128 v[112:115], v164
	s_waitcnt lgkmcnt(7)
	v_mfma_f32_16x16x32_bf16 v[72:75], v[116:119], v[20:23], v[72:75]
	v_mfma_f32_16x16x32_bf16 v[76:79], v[116:119], v[52:55], v[76:79]
	ds_read_b128 v[116:119], v164 offset:8192
	s_waitcnt lgkmcnt(7)
	v_mfma_f32_16x16x32_bf16 v[80:83], v[120:123], v[20:23], v[80:83]
	v_mfma_f32_16x16x32_bf16 v[84:87], v[120:123], v[52:55], v[84:87]
	ds_read_b128 v[120:123], v164 offset:16384
	s_waitcnt lgkmcnt(7)
	v_mfma_f32_16x16x32_bf16 v[88:91], v[124:127], v[20:23], v[88:91]
	v_mfma_f32_16x16x32_bf16 v[92:95], v[124:127], v[52:55], v[92:95]
	ds_read_b128 v[124:127], v164 offset:24576
	s_waitcnt lgkmcnt(7)
	v_mfma_f32_16x16x32_bf16 v[64:67], v[96:99], v[24:27], v[64:67]
	v_mfma_f32_16x16x32_bf16 v[68:71], v[96:99], v[56:59], v[68:71]
	s_waitcnt lgkmcnt(6)
	v_mfma_f32_16x16x32_bf16 v[72:75], v[100:103], v[24:27], v[72:75]
	v_mfma_f32_16x16x32_bf16 v[76:79], v[100:103], v[56:59], v[76:79]
	s_waitcnt lgkmcnt(5)
	v_mfma_f32_16x16x32_bf16 v[80:83], v[104:107], v[24:27], v[80:83]
	v_mfma_f32_16x16x32_bf16 v[84:87], v[104:107], v[56:59], v[84:87]
	s_waitcnt lgkmcnt(4)
	v_mfma_f32_16x16x32_bf16 v[88:91], v[108:111], v[24:27], v[88:91]
	v_mfma_f32_16x16x32_bf16 v[92:95], v[108:111], v[56:59], v[92:95]
	s_waitcnt lgkmcnt(3)
	v_mfma_f32_16x16x32_bf16 v[64:67], v[112:115], v[28:31], v[64:67]
	v_mfma_f32_16x16x32_bf16 v[68:71], v[112:115], v[60:63], v[68:71]
	s_waitcnt lgkmcnt(2)
	v_mfma_f32_16x16x32_bf16 v[72:75], v[116:119], v[28:31], v[72:75]
	v_mfma_f32_16x16x32_bf16 v[76:79], v[116:119], v[60:63], v[76:79]
	s_waitcnt lgkmcnt(1)
	v_mfma_f32_16x16x32_bf16 v[80:83], v[120:123], v[28:31], v[80:83]
	v_mfma_f32_16x16x32_bf16 v[84:87], v[120:123], v[60:63], v[84:87]
	s_waitcnt lgkmcnt(0)
	v_mfma_f32_16x16x32_bf16 v[88:91], v[124:127], v[28:31], v[88:91]
	v_mfma_f32_16x16x32_bf16 v[92:95], v[124:127], v[60:63], v[92:95]

.Lmylru_w1_7:
	v_lshlrev_b32_e32 v178, 16, v247
	v_add_f32_e32 v144, v144, v178
	v_lshlrev_b32_e32 v128, 16, v128
	v_mul_f32_e32 v144, v144, v128
	v_cvt_pk_bf16_f32 v144, v144, v144
	v_and_b32_e32 v179, 0xffff0000, v247
	v_add_f32_e32 v145, v145, v179
	v_lshlrev_b32_e32 v129, 16, v129
	v_mul_f32_e32 v145, v145, v129
	v_cvt_pk_bf16_f32 v145, v145, v145
	v_lshlrev_b32_e32 v180, 16, v248
	v_add_f32_e32 v146, v146, v180
	v_lshlrev_b32_e32 v130, 16, v130
	v_mul_f32_e32 v146, v146, v130
	v_cvt_pk_bf16_f32 v146, v146, v146
	v_and_b32_e32 v181, 0xffff0000, v248
	v_add_f32_e32 v147, v147, v181
	v_lshlrev_b32_e32 v131, 16, v131
	v_mul_f32_e32 v147, v147, v131
	v_cvt_pk_bf16_f32 v147, v147, v147
	v_lshlrev_b32_e32 v178, 16, v249
	v_add_f32_e32 v148, v148, v178
	v_lshlrev_b32_e32 v132, 16, v132
	v_mul_f32_e32 v148, v148, v132
	v_cvt_pk_bf16_f32 v148, v148, v148
	v_and_b32_e32 v179, 0xffff0000, v249
	v_add_f32_e32 v149, v149, v179
	v_lshlrev_b32_e32 v133, 16, v133
	v_mul_f32_e32 v149, v149, v133
	v_cvt_pk_bf16_f32 v149, v149, v149
	v_lshlrev_b32_e32 v180, 16, v250
	v_add_f32_e32 v150, v150, v180
	v_lshlrev_b32_e32 v134, 16, v134
	v_mul_f32_e32 v150, v150, v134
	v_cvt_pk_bf16_f32 v150, v150, v150
	v_and_b32_e32 v181, 0xffff0000, v250
	v_add_f32_e32 v151, v151, v181
	v_lshlrev_b32_e32 v135, 16, v135
	v_mul_f32_e32 v151, v151, v135
	v_cvt_pk_bf16_f32 v151, v151, v151
	v_lshlrev_b32_e32 v178, 16, v251
	v_add_f32_e32 v152, v152, v178
	v_lshlrev_b32_e32 v136, 16, v136
	v_mul_f32_e32 v152, v152, v136
	v_cvt_pk_bf16_f32 v152, v152, v152
	v_and_b32_e32 v179, 0xffff0000, v251
	v_add_f32_e32 v153, v153, v179
	v_lshlrev_b32_e32 v137, 16, v137
	v_mul_f32_e32 v153, v153, v137
	v_cvt_pk_bf16_f32 v153, v153, v153
	v_lshlrev_b32_e32 v180, 16, v252
	v_add_f32_e32 v154, v154, v180
	v_lshlrev_b32_e32 v138, 16, v138
	v_mul_f32_e32 v154, v154, v138
	v_cvt_pk_bf16_f32 v154, v154, v154
	v_and_b32_e32 v181, 0xffff0000, v252
	v_add_f32_e32 v155, v155, v181
	v_lshlrev_b32_e32 v139, 16, v139
	v_mul_f32_e32 v155, v155, v139
	v_cvt_pk_bf16_f32 v155, v155, v155
	v_lshlrev_b32_e32 v178, 16, v253
	v_add_f32_e32 v156, v156, v178
	v_lshlrev_b32_e32 v140, 16, v140
	v_mul_f32_e32 v156, v156, v140
	v_cvt_pk_bf16_f32 v156, v156, v156
	v_and_b32_e32 v179, 0xffff0000, v253
	v_add_f32_e32 v157, v157, v179
	v_lshlrev_b32_e32 v141, 16, v141
	v_mul_f32_e32 v157, v157, v141
	v_cvt_pk_bf16_f32 v157, v157, v157
	v_lshlrev_b32_e32 v180, 16, v254
	v_add_f32_e32 v158, v158, v180
	v_lshlrev_b32_e32 v142, 16, v142
	v_mul_f32_e32 v158, v158, v142
	v_cvt_pk_bf16_f32 v158, v158, v158
	v_and_b32_e32 v181, 0xffff0000, v254
	v_add_f32_e32 v159, v159, v181
	v_lshlrev_b32_e32 v143, 16, v143
	v_mul_f32_e32 v159, v159, v143
	v_cvt_pk_bf16_f32 v159, v159, v159
	v_add_u32_e32 v182, 0x0, v210
	v_add_u32_e32 v183, 0x1000, v182
	global_store_short v182, v144, s[42:43]
	global_store_short v182, v145, s[42:43] offset:2048
	global_store_short v183, v146, s[42:43]
	global_store_short v183, v147, s[42:43] offset:2048
	v_add_u32_e32 v182, 0x8000, v210
	v_add_u32_e32 v183, 0x1000, v182
	global_store_short v182, v148, s[42:43]
	global_store_short v182, v149, s[42:43] offset:2048
	global_store_short v183, v150, s[42:43]
	global_store_short v183, v151, s[42:43] offset:2048
	v_add_u32_e32 v182, 0x10000, v210
	v_add_u32_e32 v183, 0x1000, v182
	global_store_short v182, v152, s[42:43]
	global_store_short v182, v153, s[42:43] offset:2048
	global_store_short v183, v154, s[42:43]
	global_store_short v183, v155, s[42:43] offset:2048
	v_add_u32_e32 v182, 0x18000, v210
	v_add_u32_e32 v183, 0x1000, v182
	global_store_short v182, v156, s[42:43]
	global_store_short v182, v157, s[42:43] offset:2048
	global_store_short v183, v158, s[42:43]
	global_store_short v183, v159, s[42:43] offset:2048
	s_add_i32 s13, s13, 1
	s_sub_i32 s54, 17, s13
	s_lshl_b32 s55, s54, 14
	s_lshl_b32 s56, s6, 11
	s_add_i32 s55, s55, s56
	s_add_u32 s44, s22, s55
	s_addc_u32 s45, s23, 0
	s_cmp_lt_u32 s13, 2
	s_sub_i32 s50, 1, s13
	s_lshl_b32 s50, s50, 7
	s_lshl_b32 s51, s9, 8
	s_add_i32 s51, s51, 0x8000
	s_add_i32 s51, s51, s50
	s_sub_i32 s50, 17, s13
	s_lshl_b32 s50, s50, 7
	s_lshl_b32 s57, s9, 11
	s_add_i32 s57, s57, s50
	s_cmp_lt_u32 s13, 2
	s_cselect_b32 s57, s51, s57
	s_lshl_b32 s57, s57, 11
	s_add_u32 s40, s18, s57
	s_addc_u32 s41, s19, 0
	s_add_u32 s42, s20, s57
	s_addc_u32 s43, s21, 0
	global_load_dword v247, v209, s[44:45]
	global_load_dword v248, v209, s[44:45] offset:256
	global_load_dword v249, v209, s[44:45] offset:512
	global_load_dword v250, v209, s[44:45] offset:768
	global_load_dword v251, v209, s[44:45] offset:1024
	global_load_dword v252, v209, s[44:45] offset:1280
	global_load_dword v253, v209, s[44:45] offset:1536
	global_load_dword v254, v209, s[44:45] offset:1792
	v_add_u32_e32 v182, 0x0, v210
	v_add_u32_e32 v183, 0x1000, v182
	global_load_ushort v128, v182, s[40:41]
	global_load_ushort v129, v182, s[40:41] offset:2048
	global_load_ushort v130, v183, s[40:41]
	global_load_ushort v131, v183, s[40:41] offset:2048
	v_add_u32_e32 v182, 0x8000, v210
	v_add_u32_e32 v183, 0x1000, v182
	global_load_ushort v132, v182, s[40:41]
	global_load_ushort v133, v182, s[40:41] offset:2048
	global_load_ushort v134, v183, s[40:41]
	global_load_ushort v135, v183, s[40:41] offset:2048
	v_add_u32_e32 v182, 0x10000, v210
	v_add_u32_e32 v183, 0x1000, v182
	global_load_ushort v136, v182, s[40:41]
	global_load_ushort v137, v182, s[40:41] offset:2048
	global_load_ushort v138, v183, s[40:41]
	global_load_ushort v139, v183, s[40:41] offset:2048
	v_add_u32_e32 v182, 0x18000, v210
	v_add_u32_e32 v183, 0x1000, v182
	global_load_ushort v140, v182, s[40:41]
	global_load_ushort v141, v182, s[40:41] offset:2048
	global_load_ushort v142, v183, s[40:41]
	global_load_ushort v143, v183, s[40:41] offset:2048
	s_cmp_eq_u32 s14, 0
	s_cbranch_scc0 .Lmylru_nm_8
	v_or_b32_e32 v163, 0x10000, v162
	ds_read_b128 v[96:99], v163
	ds_read_b128 v[100:103], v163 offset:8192
	ds_read_b128 v[104:107], v163 offset:16384
	ds_read_b128 v[108:111], v163 offset:24576
	v_xor_b32_e32 v164, 0x40, v163
	ds_read_b128 v[112:115], v164
	ds_read_b128 v[116:119], v164 offset:8192
	ds_read_b128 v[120:123], v164 offset:16384
	ds_read_b128 v[124:127], v164 offset:24576
	s_waitcnt lgkmcnt(7)
	v_mfma_f32_16x16x32_bf16 v[64:67], v[96:99], v[0:3], 0
	v_mfma_f32_16x16x32_bf16 v[68:71], v[96:99], v[32:35], 0
	v_xor_b32_e32 v164, 0x80, v163
	ds_read_b128 v[96:99], v164
	s_waitcnt lgkmcnt(7)
	v_mfma_f32_16x16x32_bf16 v[72:75], v[100:103], v[0:3], 0
	v_mfma_f32_16x16x32_bf16 v[76:79], v[100:103], v[32:35], 0
	ds_read_b128 v[100:103], v164 offset:8192
	s_waitcnt lgkmcnt(7)
	v_mfma_f32_16x16x32_bf16 v[80:83], v[104:107], v[0:3], 0
	v_mfma_f32_16x16x32_bf16 v[84:87], v[104:107], v[32:35], 0
	ds_read_b128 v[104:107], v164 offset:16384
	s_waitcnt lgkmcnt(7)
	v_mfma_f32_16x16x32_bf16 v[88:91], v[108:111], v[0:3], 0
	v_mfma_f32_16x16x32_bf16 v[92:95], v[108:111], v[32:35], 0
	ds_read_b128 v[108:111], v164 offset:24576
	s_waitcnt lgkmcnt(7)
	v_mfma_f32_16x16x32_bf16 v[64:67], v[112:115], v[4:7], v[64:67]
	v_mfma_f32_16x16x32_bf16 v[68:71], v[112:115], v[36:39], v[68:71]
	v_xor_b32_e32 v164, 0xc0, v163
	ds_read_b128 v[112:115], v164
	s_waitcnt lgkmcnt(7)
	v_mfma_f32_16x16x32_bf16 v[72:75], v[116:119], v[4:7], v[72:75]
	v_mfma_f32_16x16x32_bf16 v[76:79], v[116:119], v[36:39], v[76:79]
	ds_read_b128 v[116:119], v164 offset:8192
	s_waitcnt lgkmcnt(7)
	v_mfma_f32_16x16x32_bf16 v[80:83], v[120:123], v[4:7], v[80:83]
	v_mfma_f32_16x16x32_bf16 v[84:87], v[120:123], v[36:39], v[84:87]
	ds_read_b128 v[120:123], v164 offset:16384
	s_waitcnt lgkmcnt(7)
	v_mfma_f32_16x16x32_bf16 v[88:91], v[124:127], v[4:7], v[88:91]
	v_mfma_f32_16x16x32_bf16 v[92:95], v[124:127], v[36:39], v[92:95]
	ds_read_b128 v[124:127], v164 offset:24576
	s_waitcnt lgkmcnt(7)
	v_mfma_f32_16x16x32_bf16 v[64:67], v[96:99], v[8:11], v[64:67]
	v_mfma_f32_16x16x32_bf16 v[68:71], v[96:99], v[40:43], v[68:71]
	v_xor_b32_e32 v164, 0x100, v163
	ds_read_b128 v[96:99], v164
	s_waitcnt lgkmcnt(7)
	v_mfma_f32_16x16x32_bf16 v[72:75], v[100:103], v[8:11], v[72:75]
	v_mfma_f32_16x16x32_bf16 v[76:79], v[100:103], v[40:43], v[76:79]
	ds_read_b128 v[100:103], v164 offset:8192
	s_waitcnt lgkmcnt(7)
	v_mfma_f32_16x16x32_bf16 v[80:83], v[104:107], v[8:11], v[80:83]
	v_mfma_f32_16x16x32_bf16 v[84:87], v[104:107], v[40:43], v[84:87]
	ds_read_b128 v[104:107], v164 offset:16384
	s_waitcnt lgkmcnt(7)
	v_mfma_f32_16x16x32_bf16 v[88:91], v[108:111], v[8:11], v[88:91]
	v_mfma_f32_16x16x32_bf16 v[92:95], v[108:111], v[40:43], v[92:95]
	ds_read_b128 v[108:111], v164 offset:24576
	s_waitcnt lgkmcnt(7)
	v_mfma_f32_16x16x32_bf16 v[64:67], v[112:115], v[12:15], v[64:67]
	v_mfma_f32_16x16x32_bf16 v[68:71], v[112:115], v[44:47], v[68:71]
	v_xor_b32_e32 v164, 0x140, v163
	ds_read_b128 v[112:115], v164
	s_waitcnt lgkmcnt(7)
	v_mfma_f32_16x16x32_bf16 v[72:75], v[116:119], v[12:15], v[72:75]
	v_mfma_f32_16x16x32_bf16 v[76:79], v[116:119], v[44:47], v[76:79]
	ds_read_b128 v[116:119], v164 offset:8192
	s_waitcnt lgkmcnt(7)
	v_mfma_f32_16x16x32_bf16 v[80:83], v[120:123], v[12:15], v[80:83]
	v_mfma_f32_16x16x32_bf16 v[84:87], v[120:123], v[44:47], v[84:87]
	ds_read_b128 v[120:123], v164 offset:16384
	s_waitcnt lgkmcnt(7)
	v_mfma_f32_16x16x32_bf16 v[88:91], v[124:127], v[12:15], v[88:91]
	v_mfma_f32_16x16x32_bf16 v[92:95], v[124:127], v[44:47], v[92:95]
	ds_read_b128 v[124:127], v164 offset:24576
	s_waitcnt lgkmcnt(7)
	v_mfma_f32_16x16x32_bf16 v[64:67], v[96:99], v[16:19], v[64:67]
	v_mfma_f32_16x16x32_bf16 v[68:71], v[96:99], v[48:51], v[68:71]
	v_xor_b32_e32 v164, 0x180, v163
	ds_read_b128 v[96:99], v164
	s_waitcnt lgkmcnt(7)
	v_mfma_f32_16x16x32_bf16 v[72:75], v[100:103], v[16:19], v[72:75]
	v_mfma_f32_16x16x32_bf16 v[76:79], v[100:103], v[48:51], v[76:79]
	ds_read_b128 v[100:103], v164 offset:8192
	s_waitcnt lgkmcnt(7)
	v_mfma_f32_16x16x32_bf16 v[80:83], v[104:107], v[16:19], v[80:83]
	v_mfma_f32_16x16x32_bf16 v[84:87], v[104:107], v[48:51], v[84:87]
	ds_read_b128 v[104:107], v164 offset:16384
	s_waitcnt lgkmcnt(7)
	v_mfma_f32_16x16x32_bf16 v[88:91], v[108:111], v[16:19], v[88:91]
	v_mfma_f32_16x16x32_bf16 v[92:95], v[108:111], v[48:51], v[92:95]
	ds_read_b128 v[108:111], v164 offset:24576
	s_waitcnt lgkmcnt(7)
	v_mfma_f32_16x16x32_bf16 v[64:67], v[112:115], v[20:23], v[64:67]
	v_mfma_f32_16x16x32_bf16 v[68:71], v[112:115], v[52:55], v[68:71]
	v_xor_b32_e32 v164, 0x1c0, v163
	ds_read_b128 v[112:115], v164
	s_waitcnt lgkmcnt(7)
	v_mfma_f32_16x16x32_bf16 v[72:75], v[116:119], v[20:23], v[72:75]
	v_mfma_f32_16x16x32_bf16 v[76:79], v[116:119], v[52:55], v[76:79]
	ds_read_b128 v[116:119], v164 offset:8192
	s_waitcnt lgkmcnt(7)
	v_mfma_f32_16x16x32_bf16 v[80:83], v[120:123], v[20:23], v[80:83]
	v_mfma_f32_16x16x32_bf16 v[84:87], v[120:123], v[52:55], v[84:87]
	ds_read_b128 v[120:123], v164 offset:16384
	s_waitcnt lgkmcnt(7)
	v_mfma_f32_16x16x32_bf16 v[88:91], v[124:127], v[20:23], v[88:91]
	v_mfma_f32_16x16x32_bf16 v[92:95], v[124:127], v[52:55], v[92:95]
	ds_read_b128 v[124:127], v164 offset:24576
	s_waitcnt lgkmcnt(7)
	v_mfma_f32_16x16x32_bf16 v[64:67], v[96:99], v[24:27], v[64:67]
	v_mfma_f32_16x16x32_bf16 v[68:71], v[96:99], v[56:59], v[68:71]
	s_waitcnt lgkmcnt(6)
	v_mfma_f32_16x16x32_bf16 v[72:75], v[100:103], v[24:27], v[72:75]
	v_mfma_f32_16x16x32_bf16 v[76:79], v[100:103], v[56:59], v[76:79]
	s_waitcnt lgkmcnt(5)
	v_mfma_f32_16x16x32_bf16 v[80:83], v[104:107], v[24:27], v[80:83]
	v_mfma_f32_16x16x32_bf16 v[84:87], v[104:107], v[56:59], v[84:87]
	s_waitcnt lgkmcnt(4)
	v_mfma_f32_16x16x32_bf16 v[88:91], v[108:111], v[24:27], v[88:91]
	v_mfma_f32_16x16x32_bf16 v[92:95], v[108:111], v[56:59], v[92:95]
	s_waitcnt lgkmcnt(3)
	v_mfma_f32_16x16x32_bf16 v[64:67], v[112:115], v[28:31], v[64:67]
	v_mfma_f32_16x16x32_bf16 v[68:71], v[112:115], v[60:63], v[68:71]
	s_waitcnt lgkmcnt(2)
	v_mfma_f32_16x16x32_bf16 v[72:75], v[116:119], v[28:31], v[72:75]
	v_mfma_f32_16x16x32_bf16 v[76:79], v[116:119], v[60:63], v[76:79]
	s_waitcnt lgkmcnt(1)
	v_mfma_f32_16x16x32_bf16 v[80:83], v[120:123], v[28:31], v[80:83]
	v_mfma_f32_16x16x32_bf16 v[84:87], v[120:123], v[60:63], v[84:87]
	s_waitcnt lgkmcnt(0)
	v_mfma_f32_16x16x32_bf16 v[88:91], v[124:127], v[28:31], v[88:91]
	v_mfma_f32_16x16x32_bf16 v[92:95], v[124:127], v[60:63], v[92:95]
